# speedup vs baseline: 1.0714x; 1.0297x over previous
.LBB1_4:
	s_or_b64 exec, exec, s[2:3]
	s_load_dwordx2 s[12:13], s[0:1], 0x0
	s_mov_b64 s[0:1], src_shared_base
	s_cmp_lg_u32 0, -1
	s_cselect_b32 s0, s1, 0
	s_cselect_b32 s1, 0, 0
	v_mov_b32_e32 v2, s1
	v_mov_b32_e32 v3, s0
	s_waitcnt lgkmcnt(0)
	s_barrier
	flat_load_dword v2, v[2:3] sc0 sc1
	s_waitcnt vmcnt(0)
	s_movk_i32 s2, 0xff
	v_cmp_lt_u32_e32 vcc, s2, v0
	v_lshlrev_b32_e32 v130, 4, v0
	v_lshrrev_b32_e32 v3, 1, v0
	v_bfe_u32 v202, v0, 5, 1
	v_and_b32_e32 v1, 3, v0
	v_and_b32_e32 v4, 64, v130
	v_and_b32_e32 v3, 12, v3
	v_and_b32_e32 v5, 0x1df0, v130
	v_mul_u32_u24_e32 v6, 0x820, v202
	v_or3_b32 v1, v1, v4, v3
	v_lshl_or_b32 v3, v202, 13, v5
	v_lshl_add_u32 v195, v1, 4, v6
	s_mov_b32 s1, 0
	s_movk_i32 s0, 0x820
	v_add_u32_e32 v1, 0, v195
	v_add_u32_e32 v194, 0, v3
	s_waitcnt lgkmcnt(0)
	s_barrier
	v_readfirstlane_b32 s14, v2
	s_ashr_i32 s2, s14, 1
	s_and_b32 s3, s14, 4
	s_and_b32 s2, s2, -8
	s_lshl_b32 s6, s14, 5
	s_or_b32 s2, s2, s3
	s_and_b32 s28, s6, 0x60
	s_ashr_i32 s33, s2, 2
	s_add_i32 s2, s33, s28
	s_ashr_i32 s3, s2, 31
	s_lshl_b64 s[20:21], s[2:3], 7
	s_bfe_u32 s29, s14, 0x10003
	v_lshrrev_b32_e32 v1, 6, v0
	v_and_b32_e32 v240, 31, v0
	v_bfe_u32 v241, v0, 5, 1
	v_readfirstlane_b32 s34, v1
	s_lshl_b32 s35, s20, 12
	s_add_u32 s40, s12, s35
	s_addc_u32 s41, s13, 0
	s_add_u32 s42, s40, 0x10000
	s_addc_u32 s43, s41, 0
	s_add_u32 s44, s42, 0x10000
	s_addc_u32 s45, s43, 0
	s_add_u32 s46, s44, 0x10000
	s_addc_u32 s47, s45, 0
	s_add_u32 s48, s46, 0x10000
	s_addc_u32 s49, s47, 0
	s_add_u32 s50, s48, 0x10000
	s_addc_u32 s51, s49, 0
	s_add_u32 s52, s50, 0x10000
	s_addc_u32 s53, s51, 0
	s_add_u32 s54, s52, 0x10000
	s_addc_u32 s55, s53, 0
	s_lshl_b32 s35, s29, 20
	s_add_u32 s56, s10, s35
	s_addc_u32 s57, s11, 0
	s_lshl_b32 s35, s34, 10
	v_lshlrev_b32_e32 v1, 4, v240
	v_lshl_add_u32 v1, v241, 13, v1
	v_add_u32_e32 v239, s35, v1
	v_bfe_u32 v1, v240, 2, 1
	v_and_b32_e32 v242, 3, v240
	v_lshrrev_b32_e32 v243, 3, v240
	v_lshl_add_u32 v242, v243, 2, v242
	v_lshl_add_u32 v1, v1, 6, v242
	v_mul_u32_u24_e32 v1, 0x110, v1
	v_lshl_add_u32 v236, v241, 4, v1
	v_lshrrev_b32_e32 v1, 5, v0
	v_lshlrev_b32_e32 v242, 12, v1
	v_lshl_add_u32 v238, v240, 4, v242
	v_mul_u32_u24_e32 v242, 0x110, v1
	v_lshl_add_u32 v237, v240, 3, v242
	s_lshl_b32 s35, s29, 9
	v_and_b32_e32 v1, 0x1c0, v0
	v_or3_b32 v1, s35, v1, v240
	v_lshlrev_b32_e32 v1, 2, v1
	global_load_dword v244, v1, s[8:9]
	global_load_dword v245, v1, s[8:9] offset:128
	global_load_dwordx4 v[204:207], v238, s[40:41]
	global_load_dwordx4 v[208:211], v238, s[42:43]
	global_load_dwordx4 v[212:215], v238, s[44:45]
	global_load_dwordx4 v[216:219], v238, s[46:47]
	global_load_dwordx4 v[220:223], v238, s[48:49]
	global_load_dwordx4 v[224:227], v238, s[50:51]
	global_load_dwordx4 v[228:231], v238, s[52:53]
	global_load_dwordx4 v[232:235], v238, s[54:55]
	global_load_dwordx4 v[146:149], v239, s[56:57]
	global_load_dwordx4 v[150:153], v239, s[56:57] offset:512
	s_add_u32 s56, s56, 0x4000
	s_addc_u32 s57, s57, 0
	global_load_dwordx4 v[154:157], v239, s[56:57]
	global_load_dwordx4 v[158:161], v239, s[56:57] offset:512
	s_add_u32 s56, s56, 0x4000
	s_addc_u32 s57, s57, 0
	global_load_dwordx4 v[162:165], v239, s[56:57]
	global_load_dwordx4 v[166:169], v239, s[56:57] offset:512
	s_add_u32 s56, s56, 0x4000
	s_addc_u32 s57, s57, 0
	global_load_dwordx4 v[170:173], v239, s[56:57]
	global_load_dwordx4 v[174:177], v239, s[56:57] offset:512
	s_add_u32 s56, s56, 0x4000
	s_addc_u32 s57, s57, 0
	global_load_dwordx4 v[178:181], v239, s[56:57]
	global_load_dwordx4 v[182:185], v239, s[56:57] offset:512
	s_add_u32 s56, s56, 0x4000
	s_addc_u32 s57, s57, 0
	s_waitcnt vmcnt(18)
	s_mov_b32 s38, 0x41a00000
	s_mov_b32 s58, 0
.Lsp_loop:
	v_mov_b32_e32 v187, v244
	v_cmp_nlt_f32_e32 vcc, s38, v187
	s_and_saveexec_b64 s[36:37], vcc
	s_cbranch_execz .Lsp_skip
	v_mul_f32_e32 v186, 0x3fb8aa3b, v187
	s_mov_b32 s39, 0x3fb8aa3b
	v_rndne_f32_e32 v188, v186
	v_sub_f32_e32 v189, v186, v188
	v_fma_f32 v186, v187, s39, -v186
	v_fmamk_f32 v186, v187, 0x32a5705f, v186
	v_add_f32_e32 v186, v189, v186
	v_exp_f32_e32 v186, v186
	v_cvt_i32_f32_e32 v188, v188
	s_mov_b32 s39, 0xc2ce8ed0
	v_cmp_ngt_f32_e32 vcc, s39, v187
	s_mov_b32 s39, 0x42b17218
	v_ldexp_f32 v186, v186, v188
	v_cndmask_b32_e32 v186, 0, v186, vcc
	v_mov_b32_e32 v200, 0x7f800000
	v_cmp_nlt_f32_e32 vcc, s39, v187
	s_mov_b32 s39, 0x3f2aaaab
	s_mov_b32 s35, 0x7f800000
	v_cndmask_b32_e32 v201, v200, v186, vcc
	v_add_f32_e32 v188, 1.0, v201
	v_add_f32_e32 v186, -1.0, v188
	v_sub_f32_e32 v187, v186, v188
	v_add_f32_e32 v187, 1.0, v187
	v_sub_f32_e32 v186, v201, v186
	v_add_f32_e32 v189, v186, v187
	v_frexp_mant_f32_e32 v190, v188
	v_cvt_f64_f32_e32 v[186:187], v188
	v_frexp_exp_i32_f64_e32 v186, v[186:187]
	v_cmp_gt_f32_e32 vcc, s39, v190
	s_mov_b32 s39, 0x3f317218
	s_nop 0
	v_subbrev_co_u32_e32 v194, vcc, 0, v186, vcc
	v_sub_u32_e32 v186, 0, v194
	v_ldexp_f32 v187, v188, v186
	v_add_f32_e32 v188, -1.0, v187
	v_add_f32_e32 v190, 1.0, v187
	v_ldexp_f32 v186, v189, v186
	v_add_f32_e32 v189, 1.0, v188
	v_add_f32_e32 v191, -1.0, v190
	v_sub_f32_e32 v189, v187, v189
	v_sub_f32_e32 v187, v187, v191
	v_add_f32_e32 v189, v186, v189
	v_add_f32_e32 v186, v186, v187
	v_add_f32_e32 v195, v190, v186
	v_rcp_f32_e32 v197, v195
	v_sub_f32_e32 v187, v190, v195
	v_add_f32_e32 v196, v186, v187
	v_add_f32_e32 v187, v188, v189
	v_mul_f32_e32 v199, v187, v197
	v_sub_f32_e32 v186, v188, v187
	v_mul_f32_e32 v188, v195, v199
	v_fma_f32 v190, v199, v195, -v188
	v_fmac_f32_e32 v190, v199, v196
	v_add_f32_e32 v198, v189, v186
	v_add_f32_e32 v186, v188, v190
	v_sub_f32_e32 v189, v187, v186
	v_pk_add_f32 v[192:193], v[186:187], v[188:189] neg_lo:[0,1] neg_hi:[0,1]
	v_mov_b32_e32 v191, v186
	v_pk_add_f32 v[186:187], v[192:193], v[190:191] neg_lo:[0,1] neg_hi:[0,1]
	v_cmp_neq_f32_e32 vcc, s35, v201
	v_add_f32_e32 v187, v198, v187
	v_add_f32_e32 v186, v186, v187
	v_add_f32_e32 v187, v189, v186
	v_mul_f32_e32 v198, v197, v187
	v_mul_f32_e32 v188, v195, v198
	v_fma_f32 v190, v198, v195, -v188
	v_fmac_f32_e32 v190, v198, v196
	v_sub_f32_e32 v189, v189, v187
	v_add_f32_e32 v195, v186, v189
	v_add_f32_e32 v186, v188, v190
	v_sub_f32_e32 v189, v187, v186
	v_pk_add_f32 v[192:193], v[186:187], v[188:189] neg_lo:[0,1] neg_hi:[0,1]
	v_mov_b32_e32 v191, v186
	v_pk_add_f32 v[186:187], v[192:193], v[190:191] neg_lo:[0,1] neg_hi:[0,1]
	v_cvt_f32_i32_e32 v188, v194
	v_add_f32_e32 v187, v195, v187
	v_add_f32_e32 v186, v186, v187
	v_add_f32_e32 v186, v189, v186
	v_add_f32_e32 v189, v199, v198
	v_sub_f32_e32 v187, v189, v199
	v_mul_f32_e32 v186, v197, v186
	v_sub_f32_e32 v187, v198, v187
	v_add_f32_e32 v186, v187, v186
	v_add_f32_e32 v190, v189, v186
	v_mul_f32_e32 v192, v190, v190
	v_mov_b32_e32 v187, 0x3ecc95a3
	v_sub_f32_e32 v189, v190, v189
	v_fmac_f32_e32 v187, 0x3e9b6dac, v192
	v_sub_f32_e32 v186, v186, v189
	v_fmaak_f32 v187, v192, v187, 0x3f2aaada
	v_ldexp_f32 v193, v186, 1
	v_mul_f32_e32 v189, v190, v192
	v_mov_b32_e32 v186, 0x3f317218
	v_pk_mul_f32 v[186:187], v[188:189], v[186:187]
	v_ldexp_f32 v191, v190, 1
	v_fma_f32 v189, v188, s39, -v186
	v_fmamk_f32 v190, v188, 0xb102e308, v189
	v_pk_add_f32 v[188:189], v[186:187], v[190:191]
	v_mov_b32_e32 v192, v186
	v_sub_f32_e32 v191, v189, v191
	v_sub_f32_e32 v191, v187, v191
	v_add_f32_e32 v193, v193, v191
	v_pk_add_f32 v[186:187], v[188:189], v[186:187] neg_lo:[0,1] neg_hi:[0,1]
	v_pk_add_f32 v[194:195], v[188:189], v[192:193]
	v_mov_b32_e32 v191, v188
	v_mov_b32_e32 v187, v195
	v_pk_add_f32 v[196:197], v[190:191], v[186:187] neg_lo:[0,1] neg_hi:[0,1]
	v_pk_add_f32 v[186:187], v[190:191], v[186:187]
	v_mov_b32_e32 v192, v193
	v_pk_add_f32 v[190:191], v[186:187], v[188:189] op_sel:[1,0] op_sel_hi:[0,1] neg_lo:[0,1] neg_hi:[0,1]
	v_pk_add_f32 v[198:199], v[194:195], v[190:191] op_sel_hi:[1,0] neg_lo:[0,1] neg_hi:[0,1]
	v_mov_b32_e32 v194, v195
	v_mov_b32_e32 v195, v187
	v_pk_mov_b32 v[190:191], v[188:189], v[190:191] op_sel:[1,0]
	v_mov_b32_e32 v193, v188
	v_pk_add_f32 v[190:191], v[194:195], v[190:191] neg_lo:[0,1] neg_hi:[0,1]
	v_mov_b32_e32 v198, v196
	v_pk_add_f32 v[188:189], v[192:193], v[190:191] neg_lo:[0,1] neg_hi:[0,1]
	v_mov_b32_e32 v197, v187
	v_pk_add_f32 v[190:191], v[198:199], v[188:189]
	s_mov_b32 s39, 0x33800000
	v_pk_add_f32 v[192:193], v[190:191], v[190:191] op_sel:[0,1] op_sel_hi:[1,0]
	s_nop 0
	v_pk_add_f32 v[186:187], v[186:187], v[192:193] op_sel:[1,0] op_sel_hi:[0,1]
	v_mov_b32_e32 v191, v186
	v_pk_add_f32 v[194:195], v[190:191], v[196:197] neg_lo:[0,1] neg_hi:[0,1]
	v_mov_b32_e32 v189, v192
	v_sub_f32_e32 v187, v190, v194
	v_pk_add_f32 v[188:189], v[188:189], v[194:195] neg_lo:[0,1] neg_hi:[0,1]
	v_sub_f32_e32 v187, v196, v187
	v_add_f32_e32 v187, v188, v187
	v_add_f32_e32 v187, v187, v189
	v_add_f32_e32 v186, v186, v187
	v_cndmask_b32_e32 v186, v200, v186, vcc
	v_cmp_lt_f32_e64 vcc, |v201|, s39
	s_nop 1
	v_cndmask_b32_e32 v187, v186, v201, vcc
.Lsp_skip:
	s_or_b64 exec, exec, s[36:37]
	v_mov_b32_e32 v244, v245
	v_mov_b32_e32 v245, v187
	s_add_u32 s58, s58, 1
	s_cmp_lt_u32 s58, 2
	s_cbranch_scc1 .Lsp_loop
	s_waitcnt vmcnt(17)
	v_cvt_pk_f16_f32 v204, v204, v205
	v_cvt_pk_f16_f32 v205, v206, v207
	ds_write_b64 v237, v[204:205]
	s_waitcnt vmcnt(16)
	v_cvt_pk_f16_f32 v208, v208, v209
	v_cvt_pk_f16_f32 v209, v210, v211
	ds_write_b64 v237, v[208:209] offset:4352
	s_waitcnt vmcnt(15)
	v_cvt_pk_f16_f32 v212, v212, v213
	v_cvt_pk_f16_f32 v213, v214, v215
	ds_write_b64 v237, v[212:213] offset:8704
	s_waitcnt vmcnt(14)
	v_cvt_pk_f16_f32 v216, v216, v217
	v_cvt_pk_f16_f32 v217, v218, v219
	ds_write_b64 v237, v[216:217] offset:13056
	s_waitcnt vmcnt(13)
	v_cvt_pk_f16_f32 v220, v220, v221
	v_cvt_pk_f16_f32 v221, v222, v223
	ds_write_b64 v237, v[220:221] offset:17408
	s_waitcnt vmcnt(12)
	v_cvt_pk_f16_f32 v224, v224, v225
	v_cvt_pk_f16_f32 v225, v226, v227
	ds_write_b64 v237, v[224:225] offset:21760
	s_waitcnt vmcnt(11)
	v_cvt_pk_f16_f32 v228, v228, v229
	v_cvt_pk_f16_f32 v229, v230, v231
	ds_write_b64 v237, v[228:229] offset:26112
	s_waitcnt vmcnt(10)
	v_cvt_pk_f16_f32 v232, v232, v233
	v_cvt_pk_f16_f32 v233, v234, v235
	ds_write_b64 v237, v[232:233] offset:30464
	global_load_dwordx4 v[204:207], v238, s[40:41] offset:512
	global_load_dwordx4 v[208:211], v238, s[42:43] offset:512
	global_load_dwordx4 v[212:215], v238, s[44:45] offset:512
	global_load_dwordx4 v[216:219], v238, s[46:47] offset:512
	global_load_dwordx4 v[220:223], v238, s[48:49] offset:512
	global_load_dwordx4 v[224:227], v238, s[50:51] offset:512
	global_load_dwordx4 v[228:231], v238, s[52:53] offset:512
	global_load_dwordx4 v[232:235], v238, s[54:55] offset:512
	s_waitcnt lgkmcnt(0)
	s_barrier
	ds_read_b128 v[130:133], v236
	ds_read_b128 v[134:137], v236 offset:4352
	ds_read_b128 v[138:141], v236 offset:8704
	ds_read_b128 v[142:145], v236 offset:13056
	s_waitcnt vmcnt(16)
	s_waitcnt lgkmcnt(3)
	v_mfma_f32_32x32x16_f16 v[82:97], v[130:133], v[146:149], 0
	v_mfma_f32_32x32x16_f16 v[50:65], v[130:133], v[150:153], 0
	ds_read_b128 v[130:133], v236 offset:32
	s_waitcnt lgkmcnt(3)
	v_mfma_f32_32x32x16_f16 v[114:129], v[134:137], v[146:149], 0
	v_mfma_f32_32x32x16_f16 v[34:49], v[134:137], v[150:153], 0
	ds_read_b128 v[134:137], v236 offset:4384
	s_waitcnt lgkmcnt(3)
	v_mfma_f32_32x32x16_f16 v[98:113], v[138:141], v[146:149], 0
	v_mfma_f32_32x32x16_f16 v[18:33], v[138:141], v[150:153], 0
	ds_read_b128 v[138:141], v236 offset:8736
	s_waitcnt lgkmcnt(3)
	v_mfma_f32_32x32x16_f16 v[66:81], v[142:145], v[146:149], 0
	v_mfma_f32_32x32x16_f16 v[2:17], v[142:145], v[150:153], 0
	ds_read_b128 v[142:145], v236 offset:13088
	global_load_dwordx4 v[146:149], v239, s[56:57]
	global_load_dwordx4 v[150:153], v239, s[56:57] offset:512
	s_add_u32 s56, s56, 0x4000
	s_addc_u32 s57, s57, 0
	s_waitcnt vmcnt(16)
	s_waitcnt lgkmcnt(3)
	v_mfma_f32_32x32x16_f16 v[82:97], v[130:133], v[154:157], v[82:97]
	v_mfma_f32_32x32x16_f16 v[50:65], v[130:133], v[158:161], v[50:65]
	ds_read_b128 v[130:133], v236 offset:64
	s_waitcnt lgkmcnt(3)
	v_mfma_f32_32x32x16_f16 v[114:129], v[134:137], v[154:157], v[114:129]
	v_mfma_f32_32x32x16_f16 v[34:49], v[134:137], v[158:161], v[34:49]
	ds_read_b128 v[134:137], v236 offset:4416
	s_waitcnt lgkmcnt(3)
	v_mfma_f32_32x32x16_f16 v[98:113], v[138:141], v[154:157], v[98:113]
	v_mfma_f32_32x32x16_f16 v[18:33], v[138:141], v[158:161], v[18:33]
	ds_read_b128 v[138:141], v236 offset:8768
	s_waitcnt lgkmcnt(3)
	v_mfma_f32_32x32x16_f16 v[66:81], v[142:145], v[154:157], v[66:81]
	v_mfma_f32_32x32x16_f16 v[2:17], v[142:145], v[158:161], v[2:17]
	ds_read_b128 v[142:145], v236 offset:13120
	global_load_dwordx4 v[154:157], v239, s[56:57]
	global_load_dwordx4 v[158:161], v239, s[56:57] offset:512
	s_add_u32 s56, s56, 0x4000
	s_addc_u32 s57, s57, 0
	s_waitcnt vmcnt(16)
	s_waitcnt lgkmcnt(3)
	v_mfma_f32_32x32x16_f16 v[82:97], v[130:133], v[162:165], v[82:97]
	v_mfma_f32_32x32x16_f16 v[50:65], v[130:133], v[166:169], v[50:65]
	ds_read_b128 v[130:133], v236 offset:96
	s_waitcnt lgkmcnt(3)
	v_mfma_f32_32x32x16_f16 v[114:129], v[134:137], v[162:165], v[114:129]
	v_mfma_f32_32x32x16_f16 v[34:49], v[134:137], v[166:169], v[34:49]
	ds_read_b128 v[134:137], v236 offset:4448
	s_waitcnt lgkmcnt(3)
	v_mfma_f32_32x32x16_f16 v[98:113], v[138:141], v[162:165], v[98:113]
	v_mfma_f32_32x32x16_f16 v[18:33], v[138:141], v[166:169], v[18:33]
	ds_read_b128 v[138:141], v236 offset:8800
	s_waitcnt lgkmcnt(3)
	v_mfma_f32_32x32x16_f16 v[66:81], v[142:145], v[162:165], v[66:81]
	v_mfma_f32_32x32x16_f16 v[2:17], v[142:145], v[166:169], v[2:17]
	ds_read_b128 v[142:145], v236 offset:13152
	global_load_dwordx4 v[162:165], v239, s[56:57]
	global_load_dwordx4 v[166:169], v239, s[56:57] offset:512
	s_add_u32 s56, s56, 0x4000
	s_addc_u32 s57, s57, 0
	s_waitcnt vmcnt(16)
	s_waitcnt lgkmcnt(3)
	v_mfma_f32_32x32x16_f16 v[82:97], v[130:133], v[170:173], v[82:97]
	v_mfma_f32_32x32x16_f16 v[50:65], v[130:133], v[174:177], v[50:65]
	ds_read_b128 v[130:133], v236 offset:128
	s_waitcnt lgkmcnt(3)
	v_mfma_f32_32x32x16_f16 v[114:129], v[134:137], v[170:173], v[114:129]
	v_mfma_f32_32x32x16_f16 v[34:49], v[134:137], v[174:177], v[34:49]
	ds_read_b128 v[134:137], v236 offset:4480
	s_waitcnt lgkmcnt(3)
	v_mfma_f32_32x32x16_f16 v[98:113], v[138:141], v[170:173], v[98:113]
	v_mfma_f32_32x32x16_f16 v[18:33], v[138:141], v[174:177], v[18:33]
	ds_read_b128 v[138:141], v236 offset:8832
	s_waitcnt lgkmcnt(3)
	v_mfma_f32_32x32x16_f16 v[66:81], v[142:145], v[170:173], v[66:81]
	v_mfma_f32_32x32x16_f16 v[2:17], v[142:145], v[174:177], v[2:17]
	ds_read_b128 v[142:145], v236 offset:13184
	global_load_dwordx4 v[170:173], v239, s[56:57]
	global_load_dwordx4 v[174:177], v239, s[56:57] offset:512
	s_add_u32 s56, s56, 0x4000
	s_addc_u32 s57, s57, 0
	s_waitcnt vmcnt(16)
	s_waitcnt lgkmcnt(3)
	v_mfma_f32_32x32x16_f16 v[82:97], v[130:133], v[178:181], v[82:97]
	v_mfma_f32_32x32x16_f16 v[50:65], v[130:133], v[182:185], v[50:65]
	ds_read_b128 v[130:133], v236 offset:160
	s_waitcnt lgkmcnt(3)
	v_mfma_f32_32x32x16_f16 v[114:129], v[134:137], v[178:181], v[114:129]
	v_mfma_f32_32x32x16_f16 v[34:49], v[134:137], v[182:185], v[34:49]
	ds_read_b128 v[134:137], v236 offset:4512
	s_waitcnt lgkmcnt(3)
	v_mfma_f32_32x32x16_f16 v[98:113], v[138:141], v[178:181], v[98:113]
	v_mfma_f32_32x32x16_f16 v[18:33], v[138:141], v[182:185], v[18:33]
	ds_read_b128 v[138:141], v236 offset:8864
	s_waitcnt lgkmcnt(3)
	v_mfma_f32_32x32x16_f16 v[66:81], v[142:145], v[178:181], v[66:81]
	v_mfma_f32_32x32x16_f16 v[2:17], v[142:145], v[182:185], v[2:17]
	ds_read_b128 v[142:145], v236 offset:13216
	global_load_dwordx4 v[178:181], v239, s[56:57]
	global_load_dwordx4 v[182:185], v239, s[56:57] offset:512
	s_add_u32 s56, s56, 0x4000
	s_addc_u32 s57, s57, 0
	s_waitcnt vmcnt(8)
	s_waitcnt lgkmcnt(3)
	v_mfma_f32_32x32x16_f16 v[82:97], v[130:133], v[146:149], v[82:97]
	v_mfma_f32_32x32x16_f16 v[50:65], v[130:133], v[150:153], v[50:65]
	ds_read_b128 v[130:133], v236 offset:192
	s_waitcnt lgkmcnt(3)
	v_mfma_f32_32x32x16_f16 v[114:129], v[134:137], v[146:149], v[114:129]
	v_mfma_f32_32x32x16_f16 v[34:49], v[134:137], v[150:153], v[34:49]
	ds_read_b128 v[134:137], v236 offset:4544
	s_waitcnt lgkmcnt(3)
	v_mfma_f32_32x32x16_f16 v[98:113], v[138:141], v[146:149], v[98:113]
	v_mfma_f32_32x32x16_f16 v[18:33], v[138:141], v[150:153], v[18:33]
	ds_read_b128 v[138:141], v236 offset:8896
	s_waitcnt lgkmcnt(3)
	v_mfma_f32_32x32x16_f16 v[66:81], v[142:145], v[146:149], v[66:81]
	v_mfma_f32_32x32x16_f16 v[2:17], v[142:145], v[150:153], v[2:17]
	ds_read_b128 v[142:145], v236 offset:13248
	global_load_dwordx4 v[146:149], v239, s[56:57]
	global_load_dwordx4 v[150:153], v239, s[56:57] offset:512
	s_add_u32 s56, s56, 0x4000
	s_addc_u32 s57, s57, 0
	s_waitcnt vmcnt(19)
	v_cvt_pk_f16_f32 v204, v204, v205
	v_cvt_pk_f16_f32 v205, v206, v207
	ds_write_b64 v237, v[204:205] offset:34816
	s_waitcnt vmcnt(18)
	v_cvt_pk_f16_f32 v208, v208, v209
	v_cvt_pk_f16_f32 v209, v210, v211
	ds_write_b64 v237, v[208:209] offset:39168
	s_waitcnt vmcnt(17)
	v_cvt_pk_f16_f32 v212, v212, v213
	v_cvt_pk_f16_f32 v213, v214, v215
	ds_write_b64 v237, v[212:213] offset:43520
	s_waitcnt vmcnt(16)
	v_cvt_pk_f16_f32 v216, v216, v217
	v_cvt_pk_f16_f32 v217, v218, v219
	ds_write_b64 v237, v[216:217] offset:47872
	s_waitcnt vmcnt(15)
	v_cvt_pk_f16_f32 v220, v220, v221
	v_cvt_pk_f16_f32 v221, v222, v223
	ds_write_b64 v237, v[220:221] offset:52224
	s_waitcnt vmcnt(14)
	v_cvt_pk_f16_f32 v224, v224, v225
	v_cvt_pk_f16_f32 v225, v226, v227
	ds_write_b64 v237, v[224:225] offset:56576
	s_waitcnt vmcnt(13)
	v_cvt_pk_f16_f32 v228, v228, v229
	v_cvt_pk_f16_f32 v229, v230, v231
	ds_write_b64 v237, v[228:229] offset:60928
	s_waitcnt vmcnt(12)
	v_cvt_pk_f16_f32 v232, v232, v233
	v_cvt_pk_f16_f32 v233, v234, v235
	ds_write_b64 v237, v[232:233] offset:65280
	global_load_dwordx4 v[204:207], v238, s[40:41] offset:1024
	global_load_dwordx4 v[208:211], v238, s[42:43] offset:1024
	global_load_dwordx4 v[212:215], v238, s[44:45] offset:1024
	global_load_dwordx4 v[216:219], v238, s[46:47] offset:1024
	global_load_dwordx4 v[220:223], v238, s[48:49] offset:1024
	global_load_dwordx4 v[224:227], v238, s[50:51] offset:1024
	global_load_dwordx4 v[228:231], v238, s[52:53] offset:1024
	global_load_dwordx4 v[232:235], v238, s[54:55] offset:1024
	s_waitcnt vmcnt(16)
	s_waitcnt lgkmcnt(11)
	v_mfma_f32_32x32x16_f16 v[82:97], v[130:133], v[154:157], v[82:97]
	v_mfma_f32_32x32x16_f16 v[50:65], v[130:133], v[158:161], v[50:65]
	ds_read_b128 v[130:133], v236 offset:224
	s_waitcnt lgkmcnt(11)
	v_mfma_f32_32x32x16_f16 v[114:129], v[134:137], v[154:157], v[114:129]
	v_mfma_f32_32x32x16_f16 v[34:49], v[134:137], v[158:161], v[34:49]
	ds_read_b128 v[134:137], v236 offset:4576
	s_waitcnt lgkmcnt(11)
	v_mfma_f32_32x32x16_f16 v[98:113], v[138:141], v[154:157], v[98:113]
	v_mfma_f32_32x32x16_f16 v[18:33], v[138:141], v[158:161], v[18:33]
	ds_read_b128 v[138:141], v236 offset:8928
	s_waitcnt lgkmcnt(11)
	v_mfma_f32_32x32x16_f16 v[66:81], v[142:145], v[154:157], v[66:81]
	v_mfma_f32_32x32x16_f16 v[2:17], v[142:145], v[158:161], v[2:17]
	ds_read_b128 v[142:145], v236 offset:13280
	global_load_dwordx4 v[154:157], v239, s[56:57]
	global_load_dwordx4 v[158:161], v239, s[56:57] offset:512
	s_add_u32 s56, s56, 0x4000
	s_addc_u32 s57, s57, 0
	s_waitcnt vmcnt(16)
	s_waitcnt lgkmcnt(3)
	v_mfma_f32_32x32x16_f16 v[82:97], v[130:133], v[162:165], v[82:97]
	v_mfma_f32_32x32x16_f16 v[50:65], v[130:133], v[166:169], v[50:65]
	s_waitcnt lgkmcnt(2)
	v_mfma_f32_32x32x16_f16 v[114:129], v[134:137], v[162:165], v[114:129]
	v_mfma_f32_32x32x16_f16 v[34:49], v[134:137], v[166:169], v[34:49]
	s_waitcnt lgkmcnt(1)
	v_mfma_f32_32x32x16_f16 v[98:113], v[138:141], v[162:165], v[98:113]
	v_mfma_f32_32x32x16_f16 v[18:33], v[138:141], v[166:169], v[18:33]
	s_waitcnt lgkmcnt(0)
	v_mfma_f32_32x32x16_f16 v[66:81], v[142:145], v[162:165], v[66:81]
	v_mfma_f32_32x32x16_f16 v[2:17], v[142:145], v[166:169], v[2:17]
	global_load_dwordx4 v[162:165], v239, s[56:57]
	global_load_dwordx4 v[166:169], v239, s[56:57] offset:512
	s_add_u32 s56, s56, 0x4000
	s_addc_u32 s57, s57, 0
	s_waitcnt lgkmcnt(0)
	s_barrier
	ds_read_b128 v[130:133], v236 offset:34816
	ds_read_b128 v[134:137], v236 offset:39168
	ds_read_b128 v[138:141], v236 offset:43520
	ds_read_b128 v[142:145], v236 offset:47872
	s_waitcnt vmcnt(16)
	s_waitcnt lgkmcnt(3)
	v_mfma_f32_32x32x16_f16 v[82:97], v[130:133], v[170:173], v[82:97]
	v_mfma_f32_32x32x16_f16 v[50:65], v[130:133], v[174:177], v[50:65]
	ds_read_b128 v[130:133], v236 offset:34848
	s_waitcnt lgkmcnt(3)
	v_mfma_f32_32x32x16_f16 v[114:129], v[134:137], v[170:173], v[114:129]
	v_mfma_f32_32x32x16_f16 v[34:49], v[134:137], v[174:177], v[34:49]
	ds_read_b128 v[134:137], v236 offset:39200
	s_waitcnt lgkmcnt(3)
	v_mfma_f32_32x32x16_f16 v[98:113], v[138:141], v[170:173], v[98:113]
	v_mfma_f32_32x32x16_f16 v[18:33], v[138:141], v[174:177], v[18:33]
	ds_read_b128 v[138:141], v236 offset:43552
	s_waitcnt lgkmcnt(3)
	v_mfma_f32_32x32x16_f16 v[66:81], v[142:145], v[170:173], v[66:81]
	v_mfma_f32_32x32x16_f16 v[2:17], v[142:145], v[174:177], v[2:17]
	ds_read_b128 v[142:145], v236 offset:47904
	global_load_dwordx4 v[170:173], v239, s[56:57]
	global_load_dwordx4 v[174:177], v239, s[56:57] offset:512
	s_add_u32 s56, s56, 0x4000
	s_addc_u32 s57, s57, 0
	s_waitcnt vmcnt(16)
	s_waitcnt lgkmcnt(3)
	v_mfma_f32_32x32x16_f16 v[82:97], v[130:133], v[178:181], v[82:97]
	v_mfma_f32_32x32x16_f16 v[50:65], v[130:133], v[182:185], v[50:65]
	ds_read_b128 v[130:133], v236 offset:34880
	s_waitcnt lgkmcnt(3)
	v_mfma_f32_32x32x16_f16 v[114:129], v[134:137], v[178:181], v[114:129]
	v_mfma_f32_32x32x16_f16 v[34:49], v[134:137], v[182:185], v[34:49]
	ds_read_b128 v[134:137], v236 offset:39232
	s_waitcnt lgkmcnt(3)
	v_mfma_f32_32x32x16_f16 v[98:113], v[138:141], v[178:181], v[98:113]
	v_mfma_f32_32x32x16_f16 v[18:33], v[138:141], v[182:185], v[18:33]
	ds_read_b128 v[138:141], v236 offset:43584
	s_waitcnt lgkmcnt(3)
	v_mfma_f32_32x32x16_f16 v[66:81], v[142:145], v[178:181], v[66:81]
	v_mfma_f32_32x32x16_f16 v[2:17], v[142:145], v[182:185], v[2:17]
	ds_read_b128 v[142:145], v236 offset:47936
	global_load_dwordx4 v[178:181], v239, s[56:57]
	global_load_dwordx4 v[182:185], v239, s[56:57] offset:512
	s_add_u32 s56, s56, 0x4000
	s_addc_u32 s57, s57, 0
	s_waitcnt vmcnt(16)
	s_waitcnt lgkmcnt(3)
	v_mfma_f32_32x32x16_f16 v[82:97], v[130:133], v[146:149], v[82:97]
	v_mfma_f32_32x32x16_f16 v[50:65], v[130:133], v[150:153], v[50:65]
	ds_read_b128 v[130:133], v236 offset:34912
	s_waitcnt lgkmcnt(3)
	v_mfma_f32_32x32x16_f16 v[114:129], v[134:137], v[146:149], v[114:129]
	v_mfma_f32_32x32x16_f16 v[34:49], v[134:137], v[150:153], v[34:49]
	ds_read_b128 v[134:137], v236 offset:39264
	s_waitcnt lgkmcnt(3)
	v_mfma_f32_32x32x16_f16 v[98:113], v[138:141], v[146:149], v[98:113]
	v_mfma_f32_32x32x16_f16 v[18:33], v[138:141], v[150:153], v[18:33]
	ds_read_b128 v[138:141], v236 offset:43616
	s_waitcnt lgkmcnt(3)
	v_mfma_f32_32x32x16_f16 v[66:81], v[142:145], v[146:149], v[66:81]
	v_mfma_f32_32x32x16_f16 v[2:17], v[142:145], v[150:153], v[2:17]
	ds_read_b128 v[142:145], v236 offset:47968
	global_load_dwordx4 v[146:149], v239, s[56:57]
	global_load_dwordx4 v[150:153], v239, s[56:57] offset:512
	s_add_u32 s56, s56, 0x4000
	s_addc_u32 s57, s57, 0
	s_waitcnt vmcnt(8)
	s_waitcnt lgkmcnt(3)
	v_mfma_f32_32x32x16_f16 v[82:97], v[130:133], v[154:157], v[82:97]
	v_mfma_f32_32x32x16_f16 v[50:65], v[130:133], v[158:161], v[50:65]
	ds_read_b128 v[130:133], v236 offset:34944
	s_waitcnt lgkmcnt(3)
	v_mfma_f32_32x32x16_f16 v[114:129], v[134:137], v[154:157], v[114:129]
	v_mfma_f32_32x32x16_f16 v[34:49], v[134:137], v[158:161], v[34:49]
	ds_read_b128 v[134:137], v236 offset:39296
	s_waitcnt lgkmcnt(3)
	v_mfma_f32_32x32x16_f16 v[98:113], v[138:141], v[154:157], v[98:113]
	v_mfma_f32_32x32x16_f16 v[18:33], v[138:141], v[158:161], v[18:33]
	ds_read_b128 v[138:141], v236 offset:43648
	s_waitcnt lgkmcnt(3)
	v_mfma_f32_32x32x16_f16 v[66:81], v[142:145], v[154:157], v[66:81]
	v_mfma_f32_32x32x16_f16 v[2:17], v[142:145], v[158:161], v[2:17]
	ds_read_b128 v[142:145], v236 offset:48000
	global_load_dwordx4 v[154:157], v239, s[56:57]
	global_load_dwordx4 v[158:161], v239, s[56:57] offset:512
	s_add_u32 s56, s56, 0x4000
	s_addc_u32 s57, s57, 0
	s_waitcnt vmcnt(8)
	s_waitcnt lgkmcnt(3)
	v_mfma_f32_32x32x16_f16 v[82:97], v[130:133], v[162:165], v[82:97]
	v_mfma_f32_32x32x16_f16 v[50:65], v[130:133], v[166:169], v[50:65]
	ds_read_b128 v[130:133], v236 offset:34976
	s_waitcnt lgkmcnt(3)
	v_mfma_f32_32x32x16_f16 v[114:129], v[134:137], v[162:165], v[114:129]
	v_mfma_f32_32x32x16_f16 v[34:49], v[134:137], v[166:169], v[34:49]
	ds_read_b128 v[134:137], v236 offset:39328
	s_waitcnt lgkmcnt(3)
	v_mfma_f32_32x32x16_f16 v[98:113], v[138:141], v[162:165], v[98:113]
	v_mfma_f32_32x32x16_f16 v[18:33], v[138:141], v[166:169], v[18:33]
	ds_read_b128 v[138:141], v236 offset:43680
	s_waitcnt lgkmcnt(3)
	v_mfma_f32_32x32x16_f16 v[66:81], v[142:145], v[162:165], v[66:81]
	v_mfma_f32_32x32x16_f16 v[2:17], v[142:145], v[166:169], v[2:17]
	ds_read_b128 v[142:145], v236 offset:48032
	global_load_dwordx4 v[162:165], v239, s[56:57]
	global_load_dwordx4 v[166:169], v239, s[56:57] offset:512
	s_add_u32 s56, s56, 0x4000
	s_addc_u32 s57, s57, 0
	s_waitcnt vmcnt(8)
	s_waitcnt lgkmcnt(3)
	v_mfma_f32_32x32x16_f16 v[82:97], v[130:133], v[170:173], v[82:97]
	v_mfma_f32_32x32x16_f16 v[50:65], v[130:133], v[174:177], v[50:65]
	ds_read_b128 v[130:133], v236 offset:35008
	s_waitcnt lgkmcnt(3)
	v_mfma_f32_32x32x16_f16 v[114:129], v[134:137], v[170:173], v[114:129]
	v_mfma_f32_32x32x16_f16 v[34:49], v[134:137], v[174:177], v[34:49]
	ds_read_b128 v[134:137], v236 offset:39360
	s_waitcnt lgkmcnt(3)
	v_mfma_f32_32x32x16_f16 v[98:113], v[138:141], v[170:173], v[98:113]
	v_mfma_f32_32x32x16_f16 v[18:33], v[138:141], v[174:177], v[18:33]
	ds_read_b128 v[138:141], v236 offset:43712
	s_waitcnt lgkmcnt(3)
	v_mfma_f32_32x32x16_f16 v[66:81], v[142:145], v[170:173], v[66:81]
	v_mfma_f32_32x32x16_f16 v[2:17], v[142:145], v[174:177], v[2:17]
	ds_read_b128 v[142:145], v236 offset:48064
	global_load_dwordx4 v[170:173], v239, s[56:57]
	global_load_dwordx4 v[174:177], v239, s[56:57] offset:512
	s_add_u32 s56, s56, 0x4000
	s_addc_u32 s57, s57, 0
	s_waitcnt vmcnt(23)
	v_cvt_pk_f16_f32 v204, v204, v205
	v_cvt_pk_f16_f32 v205, v206, v207
	ds_write_b64 v237, v[204:205]
	s_waitcnt vmcnt(22)
	v_cvt_pk_f16_f32 v208, v208, v209
	v_cvt_pk_f16_f32 v209, v210, v211
	ds_write_b64 v237, v[208:209] offset:4352
	s_waitcnt vmcnt(21)
	v_cvt_pk_f16_f32 v212, v212, v213
	v_cvt_pk_f16_f32 v213, v214, v215
	ds_write_b64 v237, v[212:213] offset:8704
	s_waitcnt vmcnt(20)
	v_cvt_pk_f16_f32 v216, v216, v217
	v_cvt_pk_f16_f32 v217, v218, v219
	ds_write_b64 v237, v[216:217] offset:13056
	s_waitcnt vmcnt(19)
	v_cvt_pk_f16_f32 v220, v220, v221
	v_cvt_pk_f16_f32 v221, v222, v223
	ds_write_b64 v237, v[220:221] offset:17408
	s_waitcnt vmcnt(18)
	v_cvt_pk_f16_f32 v224, v224, v225
	v_cvt_pk_f16_f32 v225, v226, v227
	ds_write_b64 v237, v[224:225] offset:21760
	s_waitcnt vmcnt(17)
	v_cvt_pk_f16_f32 v228, v228, v229
	v_cvt_pk_f16_f32 v229, v230, v231
	ds_write_b64 v237, v[228:229] offset:26112
	s_waitcnt vmcnt(16)
	v_cvt_pk_f16_f32 v232, v232, v233
	v_cvt_pk_f16_f32 v233, v234, v235
	ds_write_b64 v237, v[232:233] offset:30464
	global_load_dwordx4 v[204:207], v238, s[40:41] offset:1536
	global_load_dwordx4 v[208:211], v238, s[42:43] offset:1536
	global_load_dwordx4 v[212:215], v238, s[44:45] offset:1536
	global_load_dwordx4 v[216:219], v238, s[46:47] offset:1536
	global_load_dwordx4 v[220:223], v238, s[48:49] offset:1536
	global_load_dwordx4 v[224:227], v238, s[50:51] offset:1536
	global_load_dwordx4 v[228:231], v238, s[52:53] offset:1536
	global_load_dwordx4 v[232:235], v238, s[54:55] offset:1536
	s_waitcnt vmcnt(16)
	s_waitcnt lgkmcnt(11)
	v_mfma_f32_32x32x16_f16 v[82:97], v[130:133], v[178:181], v[82:97]
	v_mfma_f32_32x32x16_f16 v[50:65], v[130:133], v[182:185], v[50:65]
	ds_read_b128 v[130:133], v236 offset:35040
	s_waitcnt lgkmcnt(11)
	v_mfma_f32_32x32x16_f16 v[114:129], v[134:137], v[178:181], v[114:129]
	v_mfma_f32_32x32x16_f16 v[34:49], v[134:137], v[182:185], v[34:49]
	ds_read_b128 v[134:137], v236 offset:39392
	s_waitcnt lgkmcnt(11)
	v_mfma_f32_32x32x16_f16 v[98:113], v[138:141], v[178:181], v[98:113]
	v_mfma_f32_32x32x16_f16 v[18:33], v[138:141], v[182:185], v[18:33]
	ds_read_b128 v[138:141], v236 offset:43744
	s_waitcnt lgkmcnt(11)
	v_mfma_f32_32x32x16_f16 v[66:81], v[142:145], v[178:181], v[66:81]
	v_mfma_f32_32x32x16_f16 v[2:17], v[142:145], v[182:185], v[2:17]
	ds_read_b128 v[142:145], v236 offset:48096
	global_load_dwordx4 v[178:181], v239, s[56:57]
	global_load_dwordx4 v[182:185], v239, s[56:57] offset:512
	s_add_u32 s56, s56, 0x4000
	s_addc_u32 s57, s57, 0
	s_waitcnt vmcnt(16)
	s_waitcnt lgkmcnt(3)
	v_mfma_f32_32x32x16_f16 v[82:97], v[130:133], v[146:149], v[82:97]
	v_mfma_f32_32x32x16_f16 v[50:65], v[130:133], v[150:153], v[50:65]
	s_waitcnt lgkmcnt(2)
	v_mfma_f32_32x32x16_f16 v[114:129], v[134:137], v[146:149], v[114:129]
	v_mfma_f32_32x32x16_f16 v[34:49], v[134:137], v[150:153], v[34:49]
	s_waitcnt lgkmcnt(1)
	v_mfma_f32_32x32x16_f16 v[98:113], v[138:141], v[146:149], v[98:113]
	v_mfma_f32_32x32x16_f16 v[18:33], v[138:141], v[150:153], v[18:33]
	s_waitcnt lgkmcnt(0)
	v_mfma_f32_32x32x16_f16 v[66:81], v[142:145], v[146:149], v[66:81]
	v_mfma_f32_32x32x16_f16 v[2:17], v[142:145], v[150:153], v[2:17]
	global_load_dwordx4 v[146:149], v239, s[56:57]
	global_load_dwordx4 v[150:153], v239, s[56:57] offset:512
	s_add_u32 s56, s56, 0x4000
	s_addc_u32 s57, s57, 0
	s_waitcnt lgkmcnt(0)
	s_barrier
	ds_read_b128 v[130:133], v236
	ds_read_b128 v[134:137], v236 offset:4352
	ds_read_b128 v[138:141], v236 offset:8704
	ds_read_b128 v[142:145], v236 offset:13056
	s_waitcnt vmcnt(16)
	s_waitcnt lgkmcnt(3)
	v_mfma_f32_32x32x16_f16 v[82:97], v[130:133], v[154:157], v[82:97]
	v_mfma_f32_32x32x16_f16 v[50:65], v[130:133], v[158:161], v[50:65]
	ds_read_b128 v[130:133], v236 offset:32
	s_waitcnt lgkmcnt(3)
	v_mfma_f32_32x32x16_f16 v[114:129], v[134:137], v[154:157], v[114:129]
	v_mfma_f32_32x32x16_f16 v[34:49], v[134:137], v[158:161], v[34:49]
	ds_read_b128 v[134:137], v236 offset:4384
	s_waitcnt lgkmcnt(3)
	v_mfma_f32_32x32x16_f16 v[98:113], v[138:141], v[154:157], v[98:113]
	v_mfma_f32_32x32x16_f16 v[18:33], v[138:141], v[158:161], v[18:33]
	ds_read_b128 v[138:141], v236 offset:8736
	s_waitcnt lgkmcnt(3)
	v_mfma_f32_32x32x16_f16 v[66:81], v[142:145], v[154:157], v[66:81]
	v_mfma_f32_32x32x16_f16 v[2:17], v[142:145], v[158:161], v[2:17]
	ds_read_b128 v[142:145], v236 offset:13088
	global_load_dwordx4 v[154:157], v239, s[56:57]
	global_load_dwordx4 v[158:161], v239, s[56:57] offset:512
	s_add_u32 s56, s56, 0x4000
	s_addc_u32 s57, s57, 0
	s_waitcnt vmcnt(16)
	s_waitcnt lgkmcnt(3)
	v_mfma_f32_32x32x16_f16 v[82:97], v[130:133], v[162:165], v[82:97]
	v_mfma_f32_32x32x16_f16 v[50:65], v[130:133], v[166:169], v[50:65]
	ds_read_b128 v[130:133], v236 offset:64
	s_waitcnt lgkmcnt(3)
	v_mfma_f32_32x32x16_f16 v[114:129], v[134:137], v[162:165], v[114:129]
	v_mfma_f32_32x32x16_f16 v[34:49], v[134:137], v[166:169], v[34:49]
	ds_read_b128 v[134:137], v236 offset:4416
	s_waitcnt lgkmcnt(3)
	v_mfma_f32_32x32x16_f16 v[98:113], v[138:141], v[162:165], v[98:113]
	v_mfma_f32_32x32x16_f16 v[18:33], v[138:141], v[166:169], v[18:33]
	ds_read_b128 v[138:141], v236 offset:8768
	s_waitcnt lgkmcnt(3)
	v_mfma_f32_32x32x16_f16 v[66:81], v[142:145], v[162:165], v[66:81]
	v_mfma_f32_32x32x16_f16 v[2:17], v[142:145], v[166:169], v[2:17]
	ds_read_b128 v[142:145], v236 offset:13120
	global_load_dwordx4 v[162:165], v239, s[56:57]
	global_load_dwordx4 v[166:169], v239, s[56:57] offset:512
	s_add_u32 s56, s56, 0x4000
	s_addc_u32 s57, s57, 0
	s_waitcnt vmcnt(16)
	s_waitcnt lgkmcnt(3)
	v_mfma_f32_32x32x16_f16 v[82:97], v[130:133], v[170:173], v[82:97]
	v_mfma_f32_32x32x16_f16 v[50:65], v[130:133], v[174:177], v[50:65]
	ds_read_b128 v[130:133], v236 offset:96
	s_waitcnt lgkmcnt(3)
	v_mfma_f32_32x32x16_f16 v[114:129], v[134:137], v[170:173], v[114:129]
	v_mfma_f32_32x32x16_f16 v[34:49], v[134:137], v[174:177], v[34:49]
	ds_read_b128 v[134:137], v236 offset:4448
	s_waitcnt lgkmcnt(3)
	v_mfma_f32_32x32x16_f16 v[98:113], v[138:141], v[170:173], v[98:113]
	v_mfma_f32_32x32x16_f16 v[18:33], v[138:141], v[174:177], v[18:33]
	ds_read_b128 v[138:141], v236 offset:8800
	s_waitcnt lgkmcnt(3)
	v_mfma_f32_32x32x16_f16 v[66:81], v[142:145], v[170:173], v[66:81]
	v_mfma_f32_32x32x16_f16 v[2:17], v[142:145], v[174:177], v[2:17]
	ds_read_b128 v[142:145], v236 offset:13152
	global_load_dwordx4 v[170:173], v239, s[56:57]
	global_load_dwordx4 v[174:177], v239, s[56:57] offset:512
	s_add_u32 s56, s56, 0x4000
	s_addc_u32 s57, s57, 0
	s_waitcnt vmcnt(8)
	s_waitcnt lgkmcnt(3)
	v_mfma_f32_32x32x16_f16 v[82:97], v[130:133], v[178:181], v[82:97]
	v_mfma_f32_32x32x16_f16 v[50:65], v[130:133], v[182:185], v[50:65]
	ds_read_b128 v[130:133], v236 offset:128
	s_waitcnt lgkmcnt(3)
	v_mfma_f32_32x32x16_f16 v[114:129], v[134:137], v[178:181], v[114:129]
	v_mfma_f32_32x32x16_f16 v[34:49], v[134:137], v[182:185], v[34:49]
	ds_read_b128 v[134:137], v236 offset:4480
	s_waitcnt lgkmcnt(3)
	v_mfma_f32_32x32x16_f16 v[98:113], v[138:141], v[178:181], v[98:113]
	v_mfma_f32_32x32x16_f16 v[18:33], v[138:141], v[182:185], v[18:33]
	ds_read_b128 v[138:141], v236 offset:8832
	s_waitcnt lgkmcnt(3)
	v_mfma_f32_32x32x16_f16 v[66:81], v[142:145], v[178:181], v[66:81]
	v_mfma_f32_32x32x16_f16 v[2:17], v[142:145], v[182:185], v[2:17]
	ds_read_b128 v[142:145], v236 offset:13184
	global_load_dwordx4 v[178:181], v239, s[56:57]
	global_load_dwordx4 v[182:185], v239, s[56:57] offset:512
	s_add_u32 s56, s56, 0x4000
	s_addc_u32 s57, s57, 0
	s_waitcnt vmcnt(8)
	s_waitcnt lgkmcnt(3)
	v_mfma_f32_32x32x16_f16 v[82:97], v[130:133], v[146:149], v[82:97]
	v_mfma_f32_32x32x16_f16 v[50:65], v[130:133], v[150:153], v[50:65]
	ds_read_b128 v[130:133], v236 offset:160
	s_waitcnt lgkmcnt(3)
	v_mfma_f32_32x32x16_f16 v[114:129], v[134:137], v[146:149], v[114:129]
	v_mfma_f32_32x32x16_f16 v[34:49], v[134:137], v[150:153], v[34:49]
	ds_read_b128 v[134:137], v236 offset:4512
	s_waitcnt lgkmcnt(3)
	v_mfma_f32_32x32x16_f16 v[98:113], v[138:141], v[146:149], v[98:113]
	v_mfma_f32_32x32x16_f16 v[18:33], v[138:141], v[150:153], v[18:33]
	ds_read_b128 v[138:141], v236 offset:8864
	s_waitcnt lgkmcnt(3)
	v_mfma_f32_32x32x16_f16 v[66:81], v[142:145], v[146:149], v[66:81]
	v_mfma_f32_32x32x16_f16 v[2:17], v[142:145], v[150:153], v[2:17]
	ds_read_b128 v[142:145], v236 offset:13216
	global_load_dwordx4 v[146:149], v239, s[56:57]
	global_load_dwordx4 v[150:153], v239, s[56:57] offset:512
	s_add_u32 s56, s56, 0x4000
	s_addc_u32 s57, s57, 0
	s_waitcnt vmcnt(8)
	s_waitcnt lgkmcnt(3)
	v_mfma_f32_32x32x16_f16 v[82:97], v[130:133], v[154:157], v[82:97]
	v_mfma_f32_32x32x16_f16 v[50:65], v[130:133], v[158:161], v[50:65]
	ds_read_b128 v[130:133], v236 offset:192
	s_waitcnt lgkmcnt(3)
	v_mfma_f32_32x32x16_f16 v[114:129], v[134:137], v[154:157], v[114:129]
	v_mfma_f32_32x32x16_f16 v[34:49], v[134:137], v[158:161], v[34:49]
	ds_read_b128 v[134:137], v236 offset:4544
	s_waitcnt lgkmcnt(3)
	v_mfma_f32_32x32x16_f16 v[98:113], v[138:141], v[154:157], v[98:113]
	v_mfma_f32_32x32x16_f16 v[18:33], v[138:141], v[158:161], v[18:33]
	ds_read_b128 v[138:141], v236 offset:8896
	s_waitcnt lgkmcnt(3)
	v_mfma_f32_32x32x16_f16 v[66:81], v[142:145], v[154:157], v[66:81]
	v_mfma_f32_32x32x16_f16 v[2:17], v[142:145], v[158:161], v[2:17]
	ds_read_b128 v[142:145], v236 offset:13248
	global_load_dwordx4 v[154:157], v239, s[56:57]
	global_load_dwordx4 v[158:161], v239, s[56:57] offset:512
	s_add_u32 s56, s56, 0x4000
	s_addc_u32 s57, s57, 0
	s_waitcnt vmcnt(23)
	v_cvt_pk_f16_f32 v204, v204, v205
	v_cvt_pk_f16_f32 v205, v206, v207
	ds_write_b64 v237, v[204:205] offset:34816
	s_waitcnt vmcnt(22)
	v_cvt_pk_f16_f32 v208, v208, v209
	v_cvt_pk_f16_f32 v209, v210, v211
	ds_write_b64 v237, v[208:209] offset:39168
	s_waitcnt vmcnt(21)
	v_cvt_pk_f16_f32 v212, v212, v213
	v_cvt_pk_f16_f32 v213, v214, v215
	ds_write_b64 v237, v[212:213] offset:43520
	s_waitcnt vmcnt(20)
	v_cvt_pk_f16_f32 v216, v216, v217
	v_cvt_pk_f16_f32 v217, v218, v219
	ds_write_b64 v237, v[216:217] offset:47872
	s_waitcnt vmcnt(19)
	v_cvt_pk_f16_f32 v220, v220, v221
	v_cvt_pk_f16_f32 v221, v222, v223
	ds_write_b64 v237, v[220:221] offset:52224
	s_waitcnt vmcnt(18)
	v_cvt_pk_f16_f32 v224, v224, v225
	v_cvt_pk_f16_f32 v225, v226, v227
	ds_write_b64 v237, v[224:225] offset:56576
	s_waitcnt vmcnt(17)
	v_cvt_pk_f16_f32 v228, v228, v229
	v_cvt_pk_f16_f32 v229, v230, v231
	ds_write_b64 v237, v[228:229] offset:60928
	s_waitcnt vmcnt(16)
	v_cvt_pk_f16_f32 v232, v232, v233
	v_cvt_pk_f16_f32 v233, v234, v235
	ds_write_b64 v237, v[232:233] offset:65280
	global_load_dwordx4 v[204:207], v238, s[40:41] offset:2048
	global_load_dwordx4 v[208:211], v238, s[42:43] offset:2048
	global_load_dwordx4 v[212:215], v238, s[44:45] offset:2048
	global_load_dwordx4 v[216:219], v238, s[46:47] offset:2048
	global_load_dwordx4 v[220:223], v238, s[48:49] offset:2048
	global_load_dwordx4 v[224:227], v238, s[50:51] offset:2048
	global_load_dwordx4 v[228:231], v238, s[52:53] offset:2048
	global_load_dwordx4 v[232:235], v238, s[54:55] offset:2048
	s_waitcnt vmcnt(16)
	s_waitcnt lgkmcnt(11)
	v_mfma_f32_32x32x16_f16 v[82:97], v[130:133], v[162:165], v[82:97]
	v_mfma_f32_32x32x16_f16 v[50:65], v[130:133], v[166:169], v[50:65]
	ds_read_b128 v[130:133], v236 offset:224
	s_waitcnt lgkmcnt(11)
	v_mfma_f32_32x32x16_f16 v[114:129], v[134:137], v[162:165], v[114:129]
	v_mfma_f32_32x32x16_f16 v[34:49], v[134:137], v[166:169], v[34:49]
	ds_read_b128 v[134:137], v236 offset:4576
	s_waitcnt lgkmcnt(11)
	v_mfma_f32_32x32x16_f16 v[98:113], v[138:141], v[162:165], v[98:113]
	v_mfma_f32_32x32x16_f16 v[18:33], v[138:141], v[166:169], v[18:33]
	ds_read_b128 v[138:141], v236 offset:8928
	s_waitcnt lgkmcnt(11)
	v_mfma_f32_32x32x16_f16 v[66:81], v[142:145], v[162:165], v[66:81]
	v_mfma_f32_32x32x16_f16 v[2:17], v[142:145], v[166:169], v[2:17]
	ds_read_b128 v[142:145], v236 offset:13280
	global_load_dwordx4 v[162:165], v239, s[56:57]
	global_load_dwordx4 v[166:169], v239, s[56:57] offset:512
	s_add_u32 s56, s56, 0x4000
	s_addc_u32 s57, s57, 0
	s_waitcnt vmcnt(16)
	s_waitcnt lgkmcnt(3)
	v_mfma_f32_32x32x16_f16 v[82:97], v[130:133], v[170:173], v[82:97]
	v_mfma_f32_32x32x16_f16 v[50:65], v[130:133], v[174:177], v[50:65]
	s_waitcnt lgkmcnt(2)
	v_mfma_f32_32x32x16_f16 v[114:129], v[134:137], v[170:173], v[114:129]
	v_mfma_f32_32x32x16_f16 v[34:49], v[134:137], v[174:177], v[34:49]
	s_waitcnt lgkmcnt(1)
	v_mfma_f32_32x32x16_f16 v[98:113], v[138:141], v[170:173], v[98:113]
	v_mfma_f32_32x32x16_f16 v[18:33], v[138:141], v[174:177], v[18:33]
	s_waitcnt lgkmcnt(0)
	v_mfma_f32_32x32x16_f16 v[66:81], v[142:145], v[170:173], v[66:81]
	v_mfma_f32_32x32x16_f16 v[2:17], v[142:145], v[174:177], v[2:17]
	global_load_dwordx4 v[170:173], v239, s[56:57]
	global_load_dwordx4 v[174:177], v239, s[56:57] offset:512
	s_add_u32 s56, s56, 0x4000
	s_addc_u32 s57, s57, 0
	s_waitcnt lgkmcnt(0)
	s_barrier
	ds_read_b128 v[130:133], v236 offset:34816
	ds_read_b128 v[134:137], v236 offset:39168
	ds_read_b128 v[138:141], v236 offset:43520
	ds_read_b128 v[142:145], v236 offset:47872
	s_waitcnt vmcnt(16)
	s_waitcnt lgkmcnt(3)
	v_mfma_f32_32x32x16_f16 v[82:97], v[130:133], v[178:181], v[82:97]
	v_mfma_f32_32x32x16_f16 v[50:65], v[130:133], v[182:185], v[50:65]
	ds_read_b128 v[130:133], v236 offset:34848
	s_waitcnt lgkmcnt(3)
	v_mfma_f32_32x32x16_f16 v[114:129], v[134:137], v[178:181], v[114:129]
	v_mfma_f32_32x32x16_f16 v[34:49], v[134:137], v[182:185], v[34:49]
	ds_read_b128 v[134:137], v236 offset:39200
	s_waitcnt lgkmcnt(3)
	v_mfma_f32_32x32x16_f16 v[98:113], v[138:141], v[178:181], v[98:113]
	v_mfma_f32_32x32x16_f16 v[18:33], v[138:141], v[182:185], v[18:33]
	ds_read_b128 v[138:141], v236 offset:43552
	s_waitcnt lgkmcnt(3)
	v_mfma_f32_32x32x16_f16 v[66:81], v[142:145], v[178:181], v[66:81]
	v_mfma_f32_32x32x16_f16 v[2:17], v[142:145], v[182:185], v[2:17]
	ds_read_b128 v[142:145], v236 offset:47904
	global_load_dwordx4 v[178:181], v239, s[56:57]
	global_load_dwordx4 v[182:185], v239, s[56:57] offset:512
	s_add_u32 s56, s56, 0x4000
	s_addc_u32 s57, s57, 0
	s_waitcnt vmcnt(16)
	s_waitcnt lgkmcnt(3)
	v_mfma_f32_32x32x16_f16 v[82:97], v[130:133], v[146:149], v[82:97]
	v_mfma_f32_32x32x16_f16 v[50:65], v[130:133], v[150:153], v[50:65]
	ds_read_b128 v[130:133], v236 offset:34880
	s_waitcnt lgkmcnt(3)
	v_mfma_f32_32x32x16_f16 v[114:129], v[134:137], v[146:149], v[114:129]
	v_mfma_f32_32x32x16_f16 v[34:49], v[134:137], v[150:153], v[34:49]
	ds_read_b128 v[134:137], v236 offset:39232
	s_waitcnt lgkmcnt(3)
	v_mfma_f32_32x32x16_f16 v[98:113], v[138:141], v[146:149], v[98:113]
	v_mfma_f32_32x32x16_f16 v[18:33], v[138:141], v[150:153], v[18:33]
	ds_read_b128 v[138:141], v236 offset:43584
	s_waitcnt lgkmcnt(3)
	v_mfma_f32_32x32x16_f16 v[66:81], v[142:145], v[146:149], v[66:81]
	v_mfma_f32_32x32x16_f16 v[2:17], v[142:145], v[150:153], v[2:17]
	ds_read_b128 v[142:145], v236 offset:47936
	global_load_dwordx4 v[146:149], v239, s[56:57]
	global_load_dwordx4 v[150:153], v239, s[56:57] offset:512
	s_add_u32 s56, s56, 0x4000
	s_addc_u32 s57, s57, 0
	s_waitcnt vmcnt(16)
	s_waitcnt lgkmcnt(3)
	v_mfma_f32_32x32x16_f16 v[82:97], v[130:133], v[154:157], v[82:97]
	v_mfma_f32_32x32x16_f16 v[50:65], v[130:133], v[158:161], v[50:65]
	ds_read_b128 v[130:133], v236 offset:34912
	s_waitcnt lgkmcnt(3)
	v_mfma_f32_32x32x16_f16 v[114:129], v[134:137], v[154:157], v[114:129]
	v_mfma_f32_32x32x16_f16 v[34:49], v[134:137], v[158:161], v[34:49]
	ds_read_b128 v[134:137], v236 offset:39264
	s_waitcnt lgkmcnt(3)
	v_mfma_f32_32x32x16_f16 v[98:113], v[138:141], v[154:157], v[98:113]
	v_mfma_f32_32x32x16_f16 v[18:33], v[138:141], v[158:161], v[18:33]
	ds_read_b128 v[138:141], v236 offset:43616
	s_waitcnt lgkmcnt(3)
	v_mfma_f32_32x32x16_f16 v[66:81], v[142:145], v[154:157], v[66:81]
	v_mfma_f32_32x32x16_f16 v[2:17], v[142:145], v[158:161], v[2:17]
	ds_read_b128 v[142:145], v236 offset:47968
	global_load_dwordx4 v[154:157], v239, s[56:57]
	global_load_dwordx4 v[158:161], v239, s[56:57] offset:512
	s_add_u32 s56, s56, 0x4000
	s_addc_u32 s57, s57, 0
	s_waitcnt vmcnt(8)
	s_waitcnt lgkmcnt(3)
	v_mfma_f32_32x32x16_f16 v[82:97], v[130:133], v[162:165], v[82:97]
	v_mfma_f32_32x32x16_f16 v[50:65], v[130:133], v[166:169], v[50:65]
	ds_read_b128 v[130:133], v236 offset:34944
	s_waitcnt lgkmcnt(3)
	v_mfma_f32_32x32x16_f16 v[114:129], v[134:137], v[162:165], v[114:129]
	v_mfma_f32_32x32x16_f16 v[34:49], v[134:137], v[166:169], v[34:49]
	ds_read_b128 v[134:137], v236 offset:39296
	s_waitcnt lgkmcnt(3)
	v_mfma_f32_32x32x16_f16 v[98:113], v[138:141], v[162:165], v[98:113]
	v_mfma_f32_32x32x16_f16 v[18:33], v[138:141], v[166:169], v[18:33]
	ds_read_b128 v[138:141], v236 offset:43648
	s_waitcnt lgkmcnt(3)
	v_mfma_f32_32x32x16_f16 v[66:81], v[142:145], v[162:165], v[66:81]
	v_mfma_f32_32x32x16_f16 v[2:17], v[142:145], v[166:169], v[2:17]
	ds_read_b128 v[142:145], v236 offset:48000
	global_load_dwordx4 v[162:165], v239, s[56:57]
	global_load_dwordx4 v[166:169], v239, s[56:57] offset:512
	s_add_u32 s56, s56, 0x4000
	s_addc_u32 s57, s57, 0
	s_waitcnt vmcnt(8)
	s_waitcnt lgkmcnt(3)
	v_mfma_f32_32x32x16_f16 v[82:97], v[130:133], v[170:173], v[82:97]
	v_mfma_f32_32x32x16_f16 v[50:65], v[130:133], v[174:177], v[50:65]
	ds_read_b128 v[130:133], v236 offset:34976
	s_waitcnt lgkmcnt(3)
	v_mfma_f32_32x32x16_f16 v[114:129], v[134:137], v[170:173], v[114:129]
	v_mfma_f32_32x32x16_f16 v[34:49], v[134:137], v[174:177], v[34:49]
	ds_read_b128 v[134:137], v236 offset:39328
	s_waitcnt lgkmcnt(3)
	v_mfma_f32_32x32x16_f16 v[98:113], v[138:141], v[170:173], v[98:113]
	v_mfma_f32_32x32x16_f16 v[18:33], v[138:141], v[174:177], v[18:33]
	ds_read_b128 v[138:141], v236 offset:43680
	s_waitcnt lgkmcnt(3)
	v_mfma_f32_32x32x16_f16 v[66:81], v[142:145], v[170:173], v[66:81]
	v_mfma_f32_32x32x16_f16 v[2:17], v[142:145], v[174:177], v[2:17]
	ds_read_b128 v[142:145], v236 offset:48032
	global_load_dwordx4 v[170:173], v239, s[56:57]
	global_load_dwordx4 v[174:177], v239, s[56:57] offset:512
	s_add_u32 s56, s56, 0x4000
	s_addc_u32 s57, s57, 0
	s_waitcnt vmcnt(8)
	s_waitcnt lgkmcnt(3)
	v_mfma_f32_32x32x16_f16 v[82:97], v[130:133], v[178:181], v[82:97]
	v_mfma_f32_32x32x16_f16 v[50:65], v[130:133], v[182:185], v[50:65]
	ds_read_b128 v[130:133], v236 offset:35008
	s_waitcnt lgkmcnt(3)
	v_mfma_f32_32x32x16_f16 v[114:129], v[134:137], v[178:181], v[114:129]
	v_mfma_f32_32x32x16_f16 v[34:49], v[134:137], v[182:185], v[34:49]
	ds_read_b128 v[134:137], v236 offset:39360
	s_waitcnt lgkmcnt(3)
	v_mfma_f32_32x32x16_f16 v[98:113], v[138:141], v[178:181], v[98:113]
	v_mfma_f32_32x32x16_f16 v[18:33], v[138:141], v[182:185], v[18:33]
	ds_read_b128 v[138:141], v236 offset:43712
	s_waitcnt lgkmcnt(3)
	v_mfma_f32_32x32x16_f16 v[66:81], v[142:145], v[178:181], v[66:81]
	v_mfma_f32_32x32x16_f16 v[2:17], v[142:145], v[182:185], v[2:17]
	ds_read_b128 v[142:145], v236 offset:48064
	global_load_dwordx4 v[178:181], v239, s[56:57]
	global_load_dwordx4 v[182:185], v239, s[56:57] offset:512
	s_add_u32 s56, s56, 0x4000
	s_addc_u32 s57, s57, 0
	s_waitcnt vmcnt(23)
	v_cvt_pk_f16_f32 v204, v204, v205
	v_cvt_pk_f16_f32 v205, v206, v207
	ds_write_b64 v237, v[204:205]
	s_waitcnt vmcnt(22)
	v_cvt_pk_f16_f32 v208, v208, v209
	v_cvt_pk_f16_f32 v209, v210, v211
	ds_write_b64 v237, v[208:209] offset:4352
	s_waitcnt vmcnt(21)
	v_cvt_pk_f16_f32 v212, v212, v213
	v_cvt_pk_f16_f32 v213, v214, v215
	ds_write_b64 v237, v[212:213] offset:8704
	s_waitcnt vmcnt(20)
	v_cvt_pk_f16_f32 v216, v216, v217
	v_cvt_pk_f16_f32 v217, v218, v219
	ds_write_b64 v237, v[216:217] offset:13056
	s_waitcnt vmcnt(19)
	v_cvt_pk_f16_f32 v220, v220, v221
	v_cvt_pk_f16_f32 v221, v222, v223
	ds_write_b64 v237, v[220:221] offset:17408
	s_waitcnt vmcnt(18)
	v_cvt_pk_f16_f32 v224, v224, v225
	v_cvt_pk_f16_f32 v225, v226, v227
	ds_write_b64 v237, v[224:225] offset:21760
	s_waitcnt vmcnt(17)
	v_cvt_pk_f16_f32 v228, v228, v229
	v_cvt_pk_f16_f32 v229, v230, v231
	ds_write_b64 v237, v[228:229] offset:26112
	s_waitcnt vmcnt(16)
	v_cvt_pk_f16_f32 v232, v232, v233
	v_cvt_pk_f16_f32 v233, v234, v235
	ds_write_b64 v237, v[232:233] offset:30464
	global_load_dwordx4 v[204:207], v238, s[40:41] offset:2560
	global_load_dwordx4 v[208:211], v238, s[42:43] offset:2560
	global_load_dwordx4 v[212:215], v238, s[44:45] offset:2560
	global_load_dwordx4 v[216:219], v238, s[46:47] offset:2560
	global_load_dwordx4 v[220:223], v238, s[48:49] offset:2560
	global_load_dwordx4 v[224:227], v238, s[50:51] offset:2560
	global_load_dwordx4 v[228:231], v238, s[52:53] offset:2560
	global_load_dwordx4 v[232:235], v238, s[54:55] offset:2560
	s_waitcnt vmcnt(16)
	s_waitcnt lgkmcnt(11)
	v_mfma_f32_32x32x16_f16 v[82:97], v[130:133], v[146:149], v[82:97]
	v_mfma_f32_32x32x16_f16 v[50:65], v[130:133], v[150:153], v[50:65]
	ds_read_b128 v[130:133], v236 offset:35040
	s_waitcnt lgkmcnt(11)
	v_mfma_f32_32x32x16_f16 v[114:129], v[134:137], v[146:149], v[114:129]
	v_mfma_f32_32x32x16_f16 v[34:49], v[134:137], v[150:153], v[34:49]
	ds_read_b128 v[134:137], v236 offset:39392
	s_waitcnt lgkmcnt(11)
	v_mfma_f32_32x32x16_f16 v[98:113], v[138:141], v[146:149], v[98:113]
	v_mfma_f32_32x32x16_f16 v[18:33], v[138:141], v[150:153], v[18:33]
	ds_read_b128 v[138:141], v236 offset:43744
	s_waitcnt lgkmcnt(11)
	v_mfma_f32_32x32x16_f16 v[66:81], v[142:145], v[146:149], v[66:81]
	v_mfma_f32_32x32x16_f16 v[2:17], v[142:145], v[150:153], v[2:17]
	ds_read_b128 v[142:145], v236 offset:48096
	global_load_dwordx4 v[146:149], v239, s[56:57]
	global_load_dwordx4 v[150:153], v239, s[56:57] offset:512
	s_add_u32 s56, s56, 0x4000
	s_addc_u32 s57, s57, 0
	s_waitcnt vmcnt(16)
	s_waitcnt lgkmcnt(3)
	v_mfma_f32_32x32x16_f16 v[82:97], v[130:133], v[154:157], v[82:97]
	v_mfma_f32_32x32x16_f16 v[50:65], v[130:133], v[158:161], v[50:65]
	s_waitcnt lgkmcnt(2)
	v_mfma_f32_32x32x16_f16 v[114:129], v[134:137], v[154:157], v[114:129]
	v_mfma_f32_32x32x16_f16 v[34:49], v[134:137], v[158:161], v[34:49]
	s_waitcnt lgkmcnt(1)
	v_mfma_f32_32x32x16_f16 v[98:113], v[138:141], v[154:157], v[98:113]
	v_mfma_f32_32x32x16_f16 v[18:33], v[138:141], v[158:161], v[18:33]
	s_waitcnt lgkmcnt(0)
	v_mfma_f32_32x32x16_f16 v[66:81], v[142:145], v[154:157], v[66:81]
	v_mfma_f32_32x32x16_f16 v[2:17], v[142:145], v[158:161], v[2:17]
	global_load_dwordx4 v[154:157], v239, s[56:57]
	global_load_dwordx4 v[158:161], v239, s[56:57] offset:512
	s_add_u32 s56, s56, 0x4000
	s_addc_u32 s57, s57, 0
	s_waitcnt lgkmcnt(0)
	s_barrier
	ds_read_b128 v[130:133], v236
	ds_read_b128 v[134:137], v236 offset:4352
	ds_read_b128 v[138:141], v236 offset:8704
	ds_read_b128 v[142:145], v236 offset:13056
	s_waitcnt vmcnt(16)
	s_waitcnt lgkmcnt(3)
	v_mfma_f32_32x32x16_f16 v[82:97], v[130:133], v[162:165], v[82:97]
	v_mfma_f32_32x32x16_f16 v[50:65], v[130:133], v[166:169], v[50:65]
	ds_read_b128 v[130:133], v236 offset:32
	s_waitcnt lgkmcnt(3)
	v_mfma_f32_32x32x16_f16 v[114:129], v[134:137], v[162:165], v[114:129]
	v_mfma_f32_32x32x16_f16 v[34:49], v[134:137], v[166:169], v[34:49]
	ds_read_b128 v[134:137], v236 offset:4384
	s_waitcnt lgkmcnt(3)
	v_mfma_f32_32x32x16_f16 v[98:113], v[138:141], v[162:165], v[98:113]
	v_mfma_f32_32x32x16_f16 v[18:33], v[138:141], v[166:169], v[18:33]
	ds_read_b128 v[138:141], v236 offset:8736
	s_waitcnt lgkmcnt(3)
	v_mfma_f32_32x32x16_f16 v[66:81], v[142:145], v[162:165], v[66:81]
	v_mfma_f32_32x32x16_f16 v[2:17], v[142:145], v[166:169], v[2:17]
	ds_read_b128 v[142:145], v236 offset:13088
	global_load_dwordx4 v[162:165], v239, s[56:57]
	global_load_dwordx4 v[166:169], v239, s[56:57] offset:512
	s_add_u32 s56, s56, 0x4000
	s_addc_u32 s57, s57, 0
	s_waitcnt vmcnt(16)
	s_waitcnt lgkmcnt(3)
	v_mfma_f32_32x32x16_f16 v[82:97], v[130:133], v[170:173], v[82:97]
	v_mfma_f32_32x32x16_f16 v[50:65], v[130:133], v[174:177], v[50:65]
	ds_read_b128 v[130:133], v236 offset:64
	s_waitcnt lgkmcnt(3)
	v_mfma_f32_32x32x16_f16 v[114:129], v[134:137], v[170:173], v[114:129]
	v_mfma_f32_32x32x16_f16 v[34:49], v[134:137], v[174:177], v[34:49]
	ds_read_b128 v[134:137], v236 offset:4416
	s_waitcnt lgkmcnt(3)
	v_mfma_f32_32x32x16_f16 v[98:113], v[138:141], v[170:173], v[98:113]
	v_mfma_f32_32x32x16_f16 v[18:33], v[138:141], v[174:177], v[18:33]
	ds_read_b128 v[138:141], v236 offset:8768
	s_waitcnt lgkmcnt(3)
	v_mfma_f32_32x32x16_f16 v[66:81], v[142:145], v[170:173], v[66:81]
	v_mfma_f32_32x32x16_f16 v[2:17], v[142:145], v[174:177], v[2:17]
	ds_read_b128 v[142:145], v236 offset:13120
	global_load_dwordx4 v[170:173], v239, s[56:57]
	global_load_dwordx4 v[174:177], v239, s[56:57] offset:512
	s_add_u32 s56, s56, 0x4000
	s_addc_u32 s57, s57, 0
	s_waitcnt vmcnt(16)
	s_waitcnt lgkmcnt(3)
	v_mfma_f32_32x32x16_f16 v[82:97], v[130:133], v[178:181], v[82:97]
	v_mfma_f32_32x32x16_f16 v[50:65], v[130:133], v[182:185], v[50:65]
	ds_read_b128 v[130:133], v236 offset:96
	s_waitcnt lgkmcnt(3)
	v_mfma_f32_32x32x16_f16 v[114:129], v[134:137], v[178:181], v[114:129]
	v_mfma_f32_32x32x16_f16 v[34:49], v[134:137], v[182:185], v[34:49]
	ds_read_b128 v[134:137], v236 offset:4448
	s_waitcnt lgkmcnt(3)
	v_mfma_f32_32x32x16_f16 v[98:113], v[138:141], v[178:181], v[98:113]
	v_mfma_f32_32x32x16_f16 v[18:33], v[138:141], v[182:185], v[18:33]
	ds_read_b128 v[138:141], v236 offset:8800
	s_waitcnt lgkmcnt(3)
	v_mfma_f32_32x32x16_f16 v[66:81], v[142:145], v[178:181], v[66:81]
	v_mfma_f32_32x32x16_f16 v[2:17], v[142:145], v[182:185], v[2:17]
	ds_read_b128 v[142:145], v236 offset:13152
	global_load_dwordx4 v[178:181], v239, s[56:57]
	global_load_dwordx4 v[182:185], v239, s[56:57] offset:512
	s_add_u32 s56, s56, 0x4000
	s_addc_u32 s57, s57, 0
	s_waitcnt vmcnt(8)
	s_waitcnt lgkmcnt(3)
	v_mfma_f32_32x32x16_f16 v[82:97], v[130:133], v[146:149], v[82:97]
	v_mfma_f32_32x32x16_f16 v[50:65], v[130:133], v[150:153], v[50:65]
	ds_read_b128 v[130:133], v236 offset:128
	s_waitcnt lgkmcnt(3)
	v_mfma_f32_32x32x16_f16 v[114:129], v[134:137], v[146:149], v[114:129]
	v_mfma_f32_32x32x16_f16 v[34:49], v[134:137], v[150:153], v[34:49]
	ds_read_b128 v[134:137], v236 offset:4480
	s_waitcnt lgkmcnt(3)
	v_mfma_f32_32x32x16_f16 v[98:113], v[138:141], v[146:149], v[98:113]
	v_mfma_f32_32x32x16_f16 v[18:33], v[138:141], v[150:153], v[18:33]
	ds_read_b128 v[138:141], v236 offset:8832
	s_waitcnt lgkmcnt(3)
	v_mfma_f32_32x32x16_f16 v[66:81], v[142:145], v[146:149], v[66:81]
	v_mfma_f32_32x32x16_f16 v[2:17], v[142:145], v[150:153], v[2:17]
	ds_read_b128 v[142:145], v236 offset:13184
	global_load_dwordx4 v[146:149], v239, s[56:57]
	global_load_dwordx4 v[150:153], v239, s[56:57] offset:512
	s_add_u32 s56, s56, 0x4000
	s_addc_u32 s57, s57, 0
	s_waitcnt vmcnt(8)
	s_waitcnt lgkmcnt(3)
	v_mfma_f32_32x32x16_f16 v[82:97], v[130:133], v[154:157], v[82:97]
	v_mfma_f32_32x32x16_f16 v[50:65], v[130:133], v[158:161], v[50:65]
	ds_read_b128 v[130:133], v236 offset:160
	s_waitcnt lgkmcnt(3)
	v_mfma_f32_32x32x16_f16 v[114:129], v[134:137], v[154:157], v[114:129]
	v_mfma_f32_32x32x16_f16 v[34:49], v[134:137], v[158:161], v[34:49]
	ds_read_b128 v[134:137], v236 offset:4512
	s_waitcnt lgkmcnt(3)
	v_mfma_f32_32x32x16_f16 v[98:113], v[138:141], v[154:157], v[98:113]
	v_mfma_f32_32x32x16_f16 v[18:33], v[138:141], v[158:161], v[18:33]
	ds_read_b128 v[138:141], v236 offset:8864
	s_waitcnt lgkmcnt(3)
	v_mfma_f32_32x32x16_f16 v[66:81], v[142:145], v[154:157], v[66:81]
	v_mfma_f32_32x32x16_f16 v[2:17], v[142:145], v[158:161], v[2:17]
	ds_read_b128 v[142:145], v236 offset:13216
	global_load_dwordx4 v[154:157], v239, s[56:57]
	global_load_dwordx4 v[158:161], v239, s[56:57] offset:512
	s_add_u32 s56, s56, 0x4000
	s_addc_u32 s57, s57, 0
	s_waitcnt vmcnt(8)
	s_waitcnt lgkmcnt(3)
	v_mfma_f32_32x32x16_f16 v[82:97], v[130:133], v[162:165], v[82:97]
	v_mfma_f32_32x32x16_f16 v[50:65], v[130:133], v[166:169], v[50:65]
	ds_read_b128 v[130:133], v236 offset:192
	s_waitcnt lgkmcnt(3)
	v_mfma_f32_32x32x16_f16 v[114:129], v[134:137], v[162:165], v[114:129]
	v_mfma_f32_32x32x16_f16 v[34:49], v[134:137], v[166:169], v[34:49]
	ds_read_b128 v[134:137], v236 offset:4544
	s_waitcnt lgkmcnt(3)
	v_mfma_f32_32x32x16_f16 v[98:113], v[138:141], v[162:165], v[98:113]
	v_mfma_f32_32x32x16_f16 v[18:33], v[138:141], v[166:169], v[18:33]
	ds_read_b128 v[138:141], v236 offset:8896
	s_waitcnt lgkmcnt(3)
	v_mfma_f32_32x32x16_f16 v[66:81], v[142:145], v[162:165], v[66:81]
	v_mfma_f32_32x32x16_f16 v[2:17], v[142:145], v[166:169], v[2:17]
	ds_read_b128 v[142:145], v236 offset:13248
	global_load_dwordx4 v[162:165], v239, s[56:57]
	global_load_dwordx4 v[166:169], v239, s[56:57] offset:512
	s_add_u32 s56, s56, 0x4000
	s_addc_u32 s57, s57, 0
	s_waitcnt vmcnt(23)
	v_cvt_pk_f16_f32 v204, v204, v205
	v_cvt_pk_f16_f32 v205, v206, v207
	ds_write_b64 v237, v[204:205] offset:34816
	s_waitcnt vmcnt(22)
	v_cvt_pk_f16_f32 v208, v208, v209
	v_cvt_pk_f16_f32 v209, v210, v211
	ds_write_b64 v237, v[208:209] offset:39168
	s_waitcnt vmcnt(21)
	v_cvt_pk_f16_f32 v212, v212, v213
	v_cvt_pk_f16_f32 v213, v214, v215
	ds_write_b64 v237, v[212:213] offset:43520
	s_waitcnt vmcnt(20)
	v_cvt_pk_f16_f32 v216, v216, v217
	v_cvt_pk_f16_f32 v217, v218, v219
	ds_write_b64 v237, v[216:217] offset:47872
	s_waitcnt vmcnt(19)
	v_cvt_pk_f16_f32 v220, v220, v221
	v_cvt_pk_f16_f32 v221, v222, v223
	ds_write_b64 v237, v[220:221] offset:52224
	s_waitcnt vmcnt(18)
	v_cvt_pk_f16_f32 v224, v224, v225
	v_cvt_pk_f16_f32 v225, v226, v227
	ds_write_b64 v237, v[224:225] offset:56576
	s_waitcnt vmcnt(17)
	v_cvt_pk_f16_f32 v228, v228, v229
	v_cvt_pk_f16_f32 v229, v230, v231
	ds_write_b64 v237, v[228:229] offset:60928
	s_waitcnt vmcnt(16)
	v_cvt_pk_f16_f32 v232, v232, v233
	v_cvt_pk_f16_f32 v233, v234, v235
	ds_write_b64 v237, v[232:233] offset:65280
	global_load_dwordx4 v[204:207], v238, s[40:41] offset:3072
	global_load_dwordx4 v[208:211], v238, s[42:43] offset:3072
	global_load_dwordx4 v[212:215], v238, s[44:45] offset:3072
	global_load_dwordx4 v[216:219], v238, s[46:47] offset:3072
	global_load_dwordx4 v[220:223], v238, s[48:49] offset:3072
	global_load_dwordx4 v[224:227], v238, s[50:51] offset:3072
	global_load_dwordx4 v[228:231], v238, s[52:53] offset:3072
	global_load_dwordx4 v[232:235], v238, s[54:55] offset:3072
	s_waitcnt vmcnt(16)
	s_waitcnt lgkmcnt(11)
	v_mfma_f32_32x32x16_f16 v[82:97], v[130:133], v[170:173], v[82:97]
	v_mfma_f32_32x32x16_f16 v[50:65], v[130:133], v[174:177], v[50:65]
	ds_read_b128 v[130:133], v236 offset:224
	s_waitcnt lgkmcnt(11)
	v_mfma_f32_32x32x16_f16 v[114:129], v[134:137], v[170:173], v[114:129]
	v_mfma_f32_32x32x16_f16 v[34:49], v[134:137], v[174:177], v[34:49]
	ds_read_b128 v[134:137], v236 offset:4576
	s_waitcnt lgkmcnt(11)
	v_mfma_f32_32x32x16_f16 v[98:113], v[138:141], v[170:173], v[98:113]
	v_mfma_f32_32x32x16_f16 v[18:33], v[138:141], v[174:177], v[18:33]
	ds_read_b128 v[138:141], v236 offset:8928
	s_waitcnt lgkmcnt(11)
	v_mfma_f32_32x32x16_f16 v[66:81], v[142:145], v[170:173], v[66:81]
	v_mfma_f32_32x32x16_f16 v[2:17], v[142:145], v[174:177], v[2:17]
	ds_read_b128 v[142:145], v236 offset:13280
	global_load_dwordx4 v[170:173], v239, s[56:57]
	global_load_dwordx4 v[174:177], v239, s[56:57] offset:512
	s_add_u32 s56, s56, 0x4000
	s_addc_u32 s57, s57, 0
	s_waitcnt vmcnt(16)
	s_waitcnt lgkmcnt(3)
	v_mfma_f32_32x32x16_f16 v[82:97], v[130:133], v[178:181], v[82:97]
	v_mfma_f32_32x32x16_f16 v[50:65], v[130:133], v[182:185], v[50:65]
	s_waitcnt lgkmcnt(2)
	v_mfma_f32_32x32x16_f16 v[114:129], v[134:137], v[178:181], v[114:129]
	v_mfma_f32_32x32x16_f16 v[34:49], v[134:137], v[182:185], v[34:49]
	s_waitcnt lgkmcnt(1)
	v_mfma_f32_32x32x16_f16 v[98:113], v[138:141], v[178:181], v[98:113]
	v_mfma_f32_32x32x16_f16 v[18:33], v[138:141], v[182:185], v[18:33]
	s_waitcnt lgkmcnt(0)
	v_mfma_f32_32x32x16_f16 v[66:81], v[142:145], v[178:181], v[66:81]
	v_mfma_f32_32x32x16_f16 v[2:17], v[142:145], v[182:185], v[2:17]
	global_load_dwordx4 v[178:181], v239, s[56:57]
	global_load_dwordx4 v[182:185], v239, s[56:57] offset:512
	s_add_u32 s56, s56, 0x4000
	s_addc_u32 s57, s57, 0
	s_waitcnt lgkmcnt(0)
	s_barrier
	ds_read_b128 v[130:133], v236 offset:34816
	ds_read_b128 v[134:137], v236 offset:39168
	ds_read_b128 v[138:141], v236 offset:43520
	ds_read_b128 v[142:145], v236 offset:47872
	s_waitcnt vmcnt(16)
	s_waitcnt lgkmcnt(3)
	v_mfma_f32_32x32x16_f16 v[82:97], v[130:133], v[146:149], v[82:97]
	v_mfma_f32_32x32x16_f16 v[50:65], v[130:133], v[150:153], v[50:65]
	ds_read_b128 v[130:133], v236 offset:34848
	s_waitcnt lgkmcnt(3)
	v_mfma_f32_32x32x16_f16 v[114:129], v[134:137], v[146:149], v[114:129]
	v_mfma_f32_32x32x16_f16 v[34:49], v[134:137], v[150:153], v[34:49]
	ds_read_b128 v[134:137], v236 offset:39200
	s_waitcnt lgkmcnt(3)
	v_mfma_f32_32x32x16_f16 v[98:113], v[138:141], v[146:149], v[98:113]
	v_mfma_f32_32x32x16_f16 v[18:33], v[138:141], v[150:153], v[18:33]
	ds_read_b128 v[138:141], v236 offset:43552
	s_waitcnt lgkmcnt(3)
	v_mfma_f32_32x32x16_f16 v[66:81], v[142:145], v[146:149], v[66:81]
	v_mfma_f32_32x32x16_f16 v[2:17], v[142:145], v[150:153], v[2:17]
	ds_read_b128 v[142:145], v236 offset:47904
	global_load_dwordx4 v[146:149], v239, s[56:57]
	global_load_dwordx4 v[150:153], v239, s[56:57] offset:512
	s_add_u32 s56, s56, 0x4000
	s_addc_u32 s57, s57, 0
	s_waitcnt vmcnt(16)
	s_waitcnt lgkmcnt(3)
	v_mfma_f32_32x32x16_f16 v[82:97], v[130:133], v[154:157], v[82:97]
	v_mfma_f32_32x32x16_f16 v[50:65], v[130:133], v[158:161], v[50:65]
	ds_read_b128 v[130:133], v236 offset:34880
	s_waitcnt lgkmcnt(3)
	v_mfma_f32_32x32x16_f16 v[114:129], v[134:137], v[154:157], v[114:129]
	v_mfma_f32_32x32x16_f16 v[34:49], v[134:137], v[158:161], v[34:49]
	ds_read_b128 v[134:137], v236 offset:39232
	s_waitcnt lgkmcnt(3)
	v_mfma_f32_32x32x16_f16 v[98:113], v[138:141], v[154:157], v[98:113]
	v_mfma_f32_32x32x16_f16 v[18:33], v[138:141], v[158:161], v[18:33]
	ds_read_b128 v[138:141], v236 offset:43584
	s_waitcnt lgkmcnt(3)
	v_mfma_f32_32x32x16_f16 v[66:81], v[142:145], v[154:157], v[66:81]
	v_mfma_f32_32x32x16_f16 v[2:17], v[142:145], v[158:161], v[2:17]
	ds_read_b128 v[142:145], v236 offset:47936
	global_load_dwordx4 v[154:157], v239, s[56:57]
	global_load_dwordx4 v[158:161], v239, s[56:57] offset:512
	s_add_u32 s56, s56, 0x4000
	s_addc_u32 s57, s57, 0
	s_waitcnt vmcnt(16)
	s_waitcnt lgkmcnt(3)
	v_mfma_f32_32x32x16_f16 v[82:97], v[130:133], v[162:165], v[82:97]
	v_mfma_f32_32x32x16_f16 v[50:65], v[130:133], v[166:169], v[50:65]
	ds_read_b128 v[130:133], v236 offset:34912
	s_waitcnt lgkmcnt(3)
	v_mfma_f32_32x32x16_f16 v[114:129], v[134:137], v[162:165], v[114:129]
	v_mfma_f32_32x32x16_f16 v[34:49], v[134:137], v[166:169], v[34:49]
	ds_read_b128 v[134:137], v236 offset:39264
	s_waitcnt lgkmcnt(3)
	v_mfma_f32_32x32x16_f16 v[98:113], v[138:141], v[162:165], v[98:113]
	v_mfma_f32_32x32x16_f16 v[18:33], v[138:141], v[166:169], v[18:33]
	ds_read_b128 v[138:141], v236 offset:43616
	s_waitcnt lgkmcnt(3)
	v_mfma_f32_32x32x16_f16 v[66:81], v[142:145], v[162:165], v[66:81]
	v_mfma_f32_32x32x16_f16 v[2:17], v[142:145], v[166:169], v[2:17]
	ds_read_b128 v[142:145], v236 offset:47968
	global_load_dwordx4 v[162:165], v239, s[56:57]
	global_load_dwordx4 v[166:169], v239, s[56:57] offset:512
	s_add_u32 s56, s56, 0x4000
	s_addc_u32 s57, s57, 0
	s_waitcnt vmcnt(8)
	s_waitcnt lgkmcnt(3)
	v_mfma_f32_32x32x16_f16 v[82:97], v[130:133], v[170:173], v[82:97]
	v_mfma_f32_32x32x16_f16 v[50:65], v[130:133], v[174:177], v[50:65]
	ds_read_b128 v[130:133], v236 offset:34944
	s_waitcnt lgkmcnt(3)
	v_mfma_f32_32x32x16_f16 v[114:129], v[134:137], v[170:173], v[114:129]
	v_mfma_f32_32x32x16_f16 v[34:49], v[134:137], v[174:177], v[34:49]
	ds_read_b128 v[134:137], v236 offset:39296
	s_waitcnt lgkmcnt(3)
	v_mfma_f32_32x32x16_f16 v[98:113], v[138:141], v[170:173], v[98:113]
	v_mfma_f32_32x32x16_f16 v[18:33], v[138:141], v[174:177], v[18:33]
	ds_read_b128 v[138:141], v236 offset:43648
	s_waitcnt lgkmcnt(3)
	v_mfma_f32_32x32x16_f16 v[66:81], v[142:145], v[170:173], v[66:81]
	v_mfma_f32_32x32x16_f16 v[2:17], v[142:145], v[174:177], v[2:17]
	ds_read_b128 v[142:145], v236 offset:48000
	global_load_dwordx4 v[170:173], v239, s[56:57]
	global_load_dwordx4 v[174:177], v239, s[56:57] offset:512
	s_add_u32 s56, s56, 0x4000
	s_addc_u32 s57, s57, 0
	s_waitcnt vmcnt(8)
	s_waitcnt lgkmcnt(3)
	v_mfma_f32_32x32x16_f16 v[82:97], v[130:133], v[178:181], v[82:97]
	v_mfma_f32_32x32x16_f16 v[50:65], v[130:133], v[182:185], v[50:65]
	ds_read_b128 v[130:133], v236 offset:34976
	s_waitcnt lgkmcnt(3)
	v_mfma_f32_32x32x16_f16 v[114:129], v[134:137], v[178:181], v[114:129]
	v_mfma_f32_32x32x16_f16 v[34:49], v[134:137], v[182:185], v[34:49]
	ds_read_b128 v[134:137], v236 offset:39328
	s_waitcnt lgkmcnt(3)
	v_mfma_f32_32x32x16_f16 v[98:113], v[138:141], v[178:181], v[98:113]
	v_mfma_f32_32x32x16_f16 v[18:33], v[138:141], v[182:185], v[18:33]
	ds_read_b128 v[138:141], v236 offset:43680
	s_waitcnt lgkmcnt(3)
	v_mfma_f32_32x32x16_f16 v[66:81], v[142:145], v[178:181], v[66:81]
	v_mfma_f32_32x32x16_f16 v[2:17], v[142:145], v[182:185], v[2:17]
	ds_read_b128 v[142:145], v236 offset:48032
	global_load_dwordx4 v[178:181], v239, s[56:57]
	global_load_dwordx4 v[182:185], v239, s[56:57] offset:512
	s_add_u32 s56, s56, 0x4000
	s_addc_u32 s57, s57, 0
	s_waitcnt vmcnt(8)
	s_waitcnt lgkmcnt(3)
	v_mfma_f32_32x32x16_f16 v[82:97], v[130:133], v[146:149], v[82:97]
	v_mfma_f32_32x32x16_f16 v[50:65], v[130:133], v[150:153], v[50:65]
	ds_read_b128 v[130:133], v236 offset:35008
	s_waitcnt lgkmcnt(3)
	v_mfma_f32_32x32x16_f16 v[114:129], v[134:137], v[146:149], v[114:129]
	v_mfma_f32_32x32x16_f16 v[34:49], v[134:137], v[150:153], v[34:49]
	ds_read_b128 v[134:137], v236 offset:39360
	s_waitcnt lgkmcnt(3)
	v_mfma_f32_32x32x16_f16 v[98:113], v[138:141], v[146:149], v[98:113]
	v_mfma_f32_32x32x16_f16 v[18:33], v[138:141], v[150:153], v[18:33]
	ds_read_b128 v[138:141], v236 offset:43712
	s_waitcnt lgkmcnt(3)
	v_mfma_f32_32x32x16_f16 v[66:81], v[142:145], v[146:149], v[66:81]
	v_mfma_f32_32x32x16_f16 v[2:17], v[142:145], v[150:153], v[2:17]
	ds_read_b128 v[142:145], v236 offset:48064
	global_load_dwordx4 v[146:149], v239, s[56:57]
	global_load_dwordx4 v[150:153], v239, s[56:57] offset:512
	s_add_u32 s56, s56, 0x4000
	s_addc_u32 s57, s57, 0
	s_waitcnt vmcnt(23)
	v_cvt_pk_f16_f32 v204, v204, v205
	v_cvt_pk_f16_f32 v205, v206, v207
	ds_write_b64 v237, v[204:205]
	s_waitcnt vmcnt(22)
	v_cvt_pk_f16_f32 v208, v208, v209
	v_cvt_pk_f16_f32 v209, v210, v211
	ds_write_b64 v237, v[208:209] offset:4352
	s_waitcnt vmcnt(21)
	v_cvt_pk_f16_f32 v212, v212, v213
	v_cvt_pk_f16_f32 v213, v214, v215
	ds_write_b64 v237, v[212:213] offset:8704
	s_waitcnt vmcnt(20)
	v_cvt_pk_f16_f32 v216, v216, v217
	v_cvt_pk_f16_f32 v217, v218, v219
	ds_write_b64 v237, v[216:217] offset:13056
	s_waitcnt vmcnt(19)
	v_cvt_pk_f16_f32 v220, v220, v221
	v_cvt_pk_f16_f32 v221, v222, v223
	ds_write_b64 v237, v[220:221] offset:17408
	s_waitcnt vmcnt(18)
	v_cvt_pk_f16_f32 v224, v224, v225
	v_cvt_pk_f16_f32 v225, v226, v227
	ds_write_b64 v237, v[224:225] offset:21760
	s_waitcnt vmcnt(17)
	v_cvt_pk_f16_f32 v228, v228, v229
	v_cvt_pk_f16_f32 v229, v230, v231
	ds_write_b64 v237, v[228:229] offset:26112
	s_waitcnt vmcnt(16)
	v_cvt_pk_f16_f32 v232, v232, v233
	v_cvt_pk_f16_f32 v233, v234, v235
	ds_write_b64 v237, v[232:233] offset:30464
	global_load_dwordx4 v[204:207], v238, s[40:41] offset:3584
	global_load_dwordx4 v[208:211], v238, s[42:43] offset:3584
	global_load_dwordx4 v[212:215], v238, s[44:45] offset:3584
	global_load_dwordx4 v[216:219], v238, s[46:47] offset:3584
	global_load_dwordx4 v[220:223], v238, s[48:49] offset:3584
	global_load_dwordx4 v[224:227], v238, s[50:51] offset:3584
	global_load_dwordx4 v[228:231], v238, s[52:53] offset:3584
	global_load_dwordx4 v[232:235], v238, s[54:55] offset:3584
	s_waitcnt vmcnt(16)
	s_waitcnt lgkmcnt(11)
	v_mfma_f32_32x32x16_f16 v[82:97], v[130:133], v[154:157], v[82:97]
	v_mfma_f32_32x32x16_f16 v[50:65], v[130:133], v[158:161], v[50:65]
	ds_read_b128 v[130:133], v236 offset:35040
	s_waitcnt lgkmcnt(11)
	v_mfma_f32_32x32x16_f16 v[114:129], v[134:137], v[154:157], v[114:129]
	v_mfma_f32_32x32x16_f16 v[34:49], v[134:137], v[158:161], v[34:49]
	ds_read_b128 v[134:137], v236 offset:39392
	s_waitcnt lgkmcnt(11)
	v_mfma_f32_32x32x16_f16 v[98:113], v[138:141], v[154:157], v[98:113]
	v_mfma_f32_32x32x16_f16 v[18:33], v[138:141], v[158:161], v[18:33]
	ds_read_b128 v[138:141], v236 offset:43744
	s_waitcnt lgkmcnt(11)
	v_mfma_f32_32x32x16_f16 v[66:81], v[142:145], v[154:157], v[66:81]
	v_mfma_f32_32x32x16_f16 v[2:17], v[142:145], v[158:161], v[2:17]
	ds_read_b128 v[142:145], v236 offset:48096
	global_load_dwordx4 v[154:157], v239, s[56:57]
	global_load_dwordx4 v[158:161], v239, s[56:57] offset:512
	s_add_u32 s56, s56, 0x4000
	s_addc_u32 s57, s57, 0
	s_waitcnt vmcnt(16)
	s_waitcnt lgkmcnt(3)
	v_mfma_f32_32x32x16_f16 v[82:97], v[130:133], v[162:165], v[82:97]
	v_mfma_f32_32x32x16_f16 v[50:65], v[130:133], v[166:169], v[50:65]
	s_waitcnt lgkmcnt(2)
	v_mfma_f32_32x32x16_f16 v[114:129], v[134:137], v[162:165], v[114:129]
	v_mfma_f32_32x32x16_f16 v[34:49], v[134:137], v[166:169], v[34:49]
	s_waitcnt lgkmcnt(1)
	v_mfma_f32_32x32x16_f16 v[98:113], v[138:141], v[162:165], v[98:113]
	v_mfma_f32_32x32x16_f16 v[18:33], v[138:141], v[166:169], v[18:33]
	s_waitcnt lgkmcnt(0)
	v_mfma_f32_32x32x16_f16 v[66:81], v[142:145], v[162:165], v[66:81]
	v_mfma_f32_32x32x16_f16 v[2:17], v[142:145], v[166:169], v[2:17]
	global_load_dwordx4 v[162:165], v239, s[56:57]
	global_load_dwordx4 v[166:169], v239, s[56:57] offset:512
	s_add_u32 s56, s56, 0x4000
	s_addc_u32 s57, s57, 0
	s_waitcnt lgkmcnt(0)
	s_barrier
	ds_read_b128 v[130:133], v236
	ds_read_b128 v[134:137], v236 offset:4352
	ds_read_b128 v[138:141], v236 offset:8704
	ds_read_b128 v[142:145], v236 offset:13056
	s_waitcnt vmcnt(16)
	s_waitcnt lgkmcnt(3)
	v_mfma_f32_32x32x16_f16 v[82:97], v[130:133], v[170:173], v[82:97]
	v_mfma_f32_32x32x16_f16 v[50:65], v[130:133], v[174:177], v[50:65]
	ds_read_b128 v[130:133], v236 offset:32
	s_waitcnt lgkmcnt(3)
	v_mfma_f32_32x32x16_f16 v[114:129], v[134:137], v[170:173], v[114:129]
	v_mfma_f32_32x32x16_f16 v[34:49], v[134:137], v[174:177], v[34:49]
	ds_read_b128 v[134:137], v236 offset:4384
	s_waitcnt lgkmcnt(3)
	v_mfma_f32_32x32x16_f16 v[98:113], v[138:141], v[170:173], v[98:113]
	v_mfma_f32_32x32x16_f16 v[18:33], v[138:141], v[174:177], v[18:33]
	ds_read_b128 v[138:141], v236 offset:8736
	s_waitcnt lgkmcnt(3)
	v_mfma_f32_32x32x16_f16 v[66:81], v[142:145], v[170:173], v[66:81]
	v_mfma_f32_32x32x16_f16 v[2:17], v[142:145], v[174:177], v[2:17]
	ds_read_b128 v[142:145], v236 offset:13088
	global_load_dwordx4 v[170:173], v239, s[56:57]
	global_load_dwordx4 v[174:177], v239, s[56:57] offset:512
	s_add_u32 s56, s56, 0x4000
	s_addc_u32 s57, s57, 0
	s_waitcnt vmcnt(16)
	s_waitcnt lgkmcnt(3)
	v_mfma_f32_32x32x16_f16 v[82:97], v[130:133], v[178:181], v[82:97]
	v_mfma_f32_32x32x16_f16 v[50:65], v[130:133], v[182:185], v[50:65]
	ds_read_b128 v[130:133], v236 offset:64
	s_waitcnt lgkmcnt(3)
	v_mfma_f32_32x32x16_f16 v[114:129], v[134:137], v[178:181], v[114:129]
	v_mfma_f32_32x32x16_f16 v[34:49], v[134:137], v[182:185], v[34:49]
	ds_read_b128 v[134:137], v236 offset:4416
	s_waitcnt lgkmcnt(3)
	v_mfma_f32_32x32x16_f16 v[98:113], v[138:141], v[178:181], v[98:113]
	v_mfma_f32_32x32x16_f16 v[18:33], v[138:141], v[182:185], v[18:33]
	ds_read_b128 v[138:141], v236 offset:8768
	s_waitcnt lgkmcnt(3)
	v_mfma_f32_32x32x16_f16 v[66:81], v[142:145], v[178:181], v[66:81]
	v_mfma_f32_32x32x16_f16 v[2:17], v[142:145], v[182:185], v[2:17]
	ds_read_b128 v[142:145], v236 offset:13120
	global_load_dwordx4 v[178:181], v239, s[56:57]
	global_load_dwordx4 v[182:185], v239, s[56:57] offset:512
	s_add_u32 s56, s56, 0x4000
	s_addc_u32 s57, s57, 0
	s_waitcnt vmcnt(16)
	s_waitcnt lgkmcnt(3)
	v_mfma_f32_32x32x16_f16 v[82:97], v[130:133], v[146:149], v[82:97]
	v_mfma_f32_32x32x16_f16 v[50:65], v[130:133], v[150:153], v[50:65]
	ds_read_b128 v[130:133], v236 offset:96
	s_waitcnt lgkmcnt(3)
	v_mfma_f32_32x32x16_f16 v[114:129], v[134:137], v[146:149], v[114:129]
	v_mfma_f32_32x32x16_f16 v[34:49], v[134:137], v[150:153], v[34:49]
	ds_read_b128 v[134:137], v236 offset:4448
	s_waitcnt lgkmcnt(3)
	v_mfma_f32_32x32x16_f16 v[98:113], v[138:141], v[146:149], v[98:113]
	v_mfma_f32_32x32x16_f16 v[18:33], v[138:141], v[150:153], v[18:33]
	ds_read_b128 v[138:141], v236 offset:8800
	s_waitcnt lgkmcnt(3)
	v_mfma_f32_32x32x16_f16 v[66:81], v[142:145], v[146:149], v[66:81]
	v_mfma_f32_32x32x16_f16 v[2:17], v[142:145], v[150:153], v[2:17]
	ds_read_b128 v[142:145], v236 offset:13152
	global_load_dwordx4 v[146:149], v239, s[56:57]
	global_load_dwordx4 v[150:153], v239, s[56:57] offset:512
	s_add_u32 s56, s56, 0x4000
	s_addc_u32 s57, s57, 0
	s_waitcnt vmcnt(8)
	s_waitcnt lgkmcnt(3)
	v_mfma_f32_32x32x16_f16 v[82:97], v[130:133], v[154:157], v[82:97]
	v_mfma_f32_32x32x16_f16 v[50:65], v[130:133], v[158:161], v[50:65]
	ds_read_b128 v[130:133], v236 offset:128
	s_waitcnt lgkmcnt(3)
	v_mfma_f32_32x32x16_f16 v[114:129], v[134:137], v[154:157], v[114:129]
	v_mfma_f32_32x32x16_f16 v[34:49], v[134:137], v[158:161], v[34:49]
	ds_read_b128 v[134:137], v236 offset:4480
	s_waitcnt lgkmcnt(3)
	v_mfma_f32_32x32x16_f16 v[98:113], v[138:141], v[154:157], v[98:113]
	v_mfma_f32_32x32x16_f16 v[18:33], v[138:141], v[158:161], v[18:33]
	ds_read_b128 v[138:141], v236 offset:8832
	s_waitcnt lgkmcnt(3)
	v_mfma_f32_32x32x16_f16 v[66:81], v[142:145], v[154:157], v[66:81]
	v_mfma_f32_32x32x16_f16 v[2:17], v[142:145], v[158:161], v[2:17]
	ds_read_b128 v[142:145], v236 offset:13184
	global_load_dwordx4 v[154:157], v239, s[56:57]
	global_load_dwordx4 v[158:161], v239, s[56:57] offset:512
	s_add_u32 s56, s56, 0x4000
	s_addc_u32 s57, s57, 0
	s_waitcnt vmcnt(8)
	s_waitcnt lgkmcnt(3)
	v_mfma_f32_32x32x16_f16 v[82:97], v[130:133], v[162:165], v[82:97]
	v_mfma_f32_32x32x16_f16 v[50:65], v[130:133], v[166:169], v[50:65]
	ds_read_b128 v[130:133], v236 offset:160
	s_waitcnt lgkmcnt(3)
	v_mfma_f32_32x32x16_f16 v[114:129], v[134:137], v[162:165], v[114:129]
	v_mfma_f32_32x32x16_f16 v[34:49], v[134:137], v[166:169], v[34:49]
	ds_read_b128 v[134:137], v236 offset:4512
	s_waitcnt lgkmcnt(3)
	v_mfma_f32_32x32x16_f16 v[98:113], v[138:141], v[162:165], v[98:113]
	v_mfma_f32_32x32x16_f16 v[18:33], v[138:141], v[166:169], v[18:33]
	ds_read_b128 v[138:141], v236 offset:8864
	s_waitcnt lgkmcnt(3)
	v_mfma_f32_32x32x16_f16 v[66:81], v[142:145], v[162:165], v[66:81]
	v_mfma_f32_32x32x16_f16 v[2:17], v[142:145], v[166:169], v[2:17]
	ds_read_b128 v[142:145], v236 offset:13216
	global_load_dwordx4 v[162:165], v239, s[56:57]
	global_load_dwordx4 v[166:169], v239, s[56:57] offset:512
	s_add_u32 s56, s56, 0x4000
	s_addc_u32 s57, s57, 0
	s_waitcnt vmcnt(8)
	s_waitcnt lgkmcnt(3)
	v_mfma_f32_32x32x16_f16 v[82:97], v[130:133], v[170:173], v[82:97]
	v_mfma_f32_32x32x16_f16 v[50:65], v[130:133], v[174:177], v[50:65]
	ds_read_b128 v[130:133], v236 offset:192
	s_waitcnt lgkmcnt(3)
	v_mfma_f32_32x32x16_f16 v[114:129], v[134:137], v[170:173], v[114:129]
	v_mfma_f32_32x32x16_f16 v[34:49], v[134:137], v[174:177], v[34:49]
	ds_read_b128 v[134:137], v236 offset:4544
	s_waitcnt lgkmcnt(3)
	v_mfma_f32_32x32x16_f16 v[98:113], v[138:141], v[170:173], v[98:113]
	v_mfma_f32_32x32x16_f16 v[18:33], v[138:141], v[174:177], v[18:33]
	ds_read_b128 v[138:141], v236 offset:8896
	s_waitcnt lgkmcnt(3)
	v_mfma_f32_32x32x16_f16 v[66:81], v[142:145], v[170:173], v[66:81]
	v_mfma_f32_32x32x16_f16 v[2:17], v[142:145], v[174:177], v[2:17]
	ds_read_b128 v[142:145], v236 offset:13248
	global_load_dwordx4 v[170:173], v239, s[56:57]
	global_load_dwordx4 v[174:177], v239, s[56:57] offset:512
	s_add_u32 s56, s56, 0x4000
	s_addc_u32 s57, s57, 0
	s_waitcnt vmcnt(23)
	v_cvt_pk_f16_f32 v204, v204, v205
	v_cvt_pk_f16_f32 v205, v206, v207
	ds_write_b64 v237, v[204:205] offset:34816
	s_waitcnt vmcnt(22)
	v_cvt_pk_f16_f32 v208, v208, v209
	v_cvt_pk_f16_f32 v209, v210, v211
	ds_write_b64 v237, v[208:209] offset:39168
	s_waitcnt vmcnt(21)
	v_cvt_pk_f16_f32 v212, v212, v213
	v_cvt_pk_f16_f32 v213, v214, v215
	ds_write_b64 v237, v[212:213] offset:43520
	s_waitcnt vmcnt(20)
	v_cvt_pk_f16_f32 v216, v216, v217
	v_cvt_pk_f16_f32 v217, v218, v219
	ds_write_b64 v237, v[216:217] offset:47872
	s_waitcnt vmcnt(19)
	v_cvt_pk_f16_f32 v220, v220, v221
	v_cvt_pk_f16_f32 v221, v222, v223
	ds_write_b64 v237, v[220:221] offset:52224
	s_waitcnt vmcnt(18)
	v_cvt_pk_f16_f32 v224, v224, v225
	v_cvt_pk_f16_f32 v225, v226, v227
	ds_write_b64 v237, v[224:225] offset:56576
	s_waitcnt vmcnt(17)
	v_cvt_pk_f16_f32 v228, v228, v229
	v_cvt_pk_f16_f32 v229, v230, v231
	ds_write_b64 v237, v[228:229] offset:60928
	s_waitcnt vmcnt(16)
	v_cvt_pk_f16_f32 v232, v232, v233
	v_cvt_pk_f16_f32 v233, v234, v235
	ds_write_b64 v237, v[232:233] offset:65280
	s_waitcnt vmcnt(8)
	s_waitcnt lgkmcnt(11)
	v_mfma_f32_32x32x16_f16 v[82:97], v[130:133], v[178:181], v[82:97]
	v_mfma_f32_32x32x16_f16 v[50:65], v[130:133], v[182:185], v[50:65]
	ds_read_b128 v[130:133], v236 offset:224
	s_waitcnt lgkmcnt(11)
	v_mfma_f32_32x32x16_f16 v[114:129], v[134:137], v[178:181], v[114:129]
	v_mfma_f32_32x32x16_f16 v[34:49], v[134:137], v[182:185], v[34:49]
	ds_read_b128 v[134:137], v236 offset:4576
	s_waitcnt lgkmcnt(11)
	v_mfma_f32_32x32x16_f16 v[98:113], v[138:141], v[178:181], v[98:113]
	v_mfma_f32_32x32x16_f16 v[18:33], v[138:141], v[182:185], v[18:33]
	ds_read_b128 v[138:141], v236 offset:8928
	s_waitcnt lgkmcnt(11)
	v_mfma_f32_32x32x16_f16 v[66:81], v[142:145], v[178:181], v[66:81]
	v_mfma_f32_32x32x16_f16 v[2:17], v[142:145], v[182:185], v[2:17]
	ds_read_b128 v[142:145], v236 offset:13280
	global_load_dwordx4 v[178:181], v239, s[56:57]
	global_load_dwordx4 v[182:185], v239, s[56:57] offset:512
	s_add_u32 s56, s56, 0x4000
	s_addc_u32 s57, s57, 0
	s_waitcnt vmcnt(8)
	s_waitcnt lgkmcnt(3)
	v_mfma_f32_32x32x16_f16 v[82:97], v[130:133], v[146:149], v[82:97]
	v_mfma_f32_32x32x16_f16 v[50:65], v[130:133], v[150:153], v[50:65]
	s_waitcnt lgkmcnt(2)
	v_mfma_f32_32x32x16_f16 v[114:129], v[134:137], v[146:149], v[114:129]
	v_mfma_f32_32x32x16_f16 v[34:49], v[134:137], v[150:153], v[34:49]
	s_waitcnt lgkmcnt(1)
	v_mfma_f32_32x32x16_f16 v[98:113], v[138:141], v[146:149], v[98:113]
	v_mfma_f32_32x32x16_f16 v[18:33], v[138:141], v[150:153], v[18:33]
	s_waitcnt lgkmcnt(0)
	v_mfma_f32_32x32x16_f16 v[66:81], v[142:145], v[146:149], v[66:81]
	v_mfma_f32_32x32x16_f16 v[2:17], v[142:145], v[150:153], v[2:17]
	global_load_dwordx4 v[146:149], v239, s[56:57]
	global_load_dwordx4 v[150:153], v239, s[56:57] offset:512
	s_add_u32 s56, s56, 0x4000
	s_addc_u32 s57, s57, 0
	s_waitcnt lgkmcnt(0)
	s_barrier
	ds_read_b128 v[130:133], v236 offset:34816
	ds_read_b128 v[134:137], v236 offset:39168
	ds_read_b128 v[138:141], v236 offset:43520
	ds_read_b128 v[142:145], v236 offset:47872
	s_waitcnt vmcnt(8)
	s_waitcnt lgkmcnt(3)
	v_mfma_f32_32x32x16_f16 v[82:97], v[130:133], v[154:157], v[82:97]
	v_mfma_f32_32x32x16_f16 v[50:65], v[130:133], v[158:161], v[50:65]
	ds_read_b128 v[130:133], v236 offset:34848
	s_waitcnt lgkmcnt(3)
	v_mfma_f32_32x32x16_f16 v[114:129], v[134:137], v[154:157], v[114:129]
	v_mfma_f32_32x32x16_f16 v[34:49], v[134:137], v[158:161], v[34:49]
	ds_read_b128 v[134:137], v236 offset:39200
	s_waitcnt lgkmcnt(3)
	v_mfma_f32_32x32x16_f16 v[98:113], v[138:141], v[154:157], v[98:113]
	v_mfma_f32_32x32x16_f16 v[18:33], v[138:141], v[158:161], v[18:33]
	ds_read_b128 v[138:141], v236 offset:43552
	s_waitcnt lgkmcnt(3)
	v_mfma_f32_32x32x16_f16 v[66:81], v[142:145], v[154:157], v[66:81]
	v_mfma_f32_32x32x16_f16 v[2:17], v[142:145], v[158:161], v[2:17]
	ds_read_b128 v[142:145], v236 offset:47904
	global_load_dwordx4 v[154:157], v239, s[56:57]
	global_load_dwordx4 v[158:161], v239, s[56:57] offset:512
	s_add_u32 s56, s56, 0x4000
	s_addc_u32 s57, s57, 0
	s_waitcnt vmcnt(8)
	s_waitcnt lgkmcnt(3)
	v_mfma_f32_32x32x16_f16 v[82:97], v[130:133], v[162:165], v[82:97]
	v_mfma_f32_32x32x16_f16 v[50:65], v[130:133], v[166:169], v[50:65]
	ds_read_b128 v[130:133], v236 offset:34880
	s_waitcnt lgkmcnt(3)
	v_mfma_f32_32x32x16_f16 v[114:129], v[134:137], v[162:165], v[114:129]
	v_mfma_f32_32x32x16_f16 v[34:49], v[134:137], v[166:169], v[34:49]
	ds_read_b128 v[134:137], v236 offset:39232
	s_waitcnt lgkmcnt(3)
	v_mfma_f32_32x32x16_f16 v[98:113], v[138:141], v[162:165], v[98:113]
	v_mfma_f32_32x32x16_f16 v[18:33], v[138:141], v[166:169], v[18:33]
	ds_read_b128 v[138:141], v236 offset:43584
	s_waitcnt lgkmcnt(3)
	v_mfma_f32_32x32x16_f16 v[66:81], v[142:145], v[162:165], v[66:81]
	v_mfma_f32_32x32x16_f16 v[2:17], v[142:145], v[166:169], v[2:17]
	ds_read_b128 v[142:145], v236 offset:47936
	global_load_dwordx4 v[162:165], v239, s[56:57]
	global_load_dwordx4 v[166:169], v239, s[56:57] offset:512
	s_add_u32 s56, s56, 0x4000
	s_addc_u32 s57, s57, 0
	s_waitcnt vmcnt(8)
	s_waitcnt lgkmcnt(3)
	v_mfma_f32_32x32x16_f16 v[82:97], v[130:133], v[170:173], v[82:97]
	v_mfma_f32_32x32x16_f16 v[50:65], v[130:133], v[174:177], v[50:65]
	ds_read_b128 v[130:133], v236 offset:34912
	s_waitcnt lgkmcnt(3)
	v_mfma_f32_32x32x16_f16 v[114:129], v[134:137], v[170:173], v[114:129]
	v_mfma_f32_32x32x16_f16 v[34:49], v[134:137], v[174:177], v[34:49]
	ds_read_b128 v[134:137], v236 offset:39264
	s_waitcnt lgkmcnt(3)
	v_mfma_f32_32x32x16_f16 v[98:113], v[138:141], v[170:173], v[98:113]
	v_mfma_f32_32x32x16_f16 v[18:33], v[138:141], v[174:177], v[18:33]
	ds_read_b128 v[138:141], v236 offset:43616
	s_waitcnt lgkmcnt(3)
	v_mfma_f32_32x32x16_f16 v[66:81], v[142:145], v[170:173], v[66:81]
	v_mfma_f32_32x32x16_f16 v[2:17], v[142:145], v[174:177], v[2:17]
	ds_read_b128 v[142:145], v236 offset:47968
	global_load_dwordx4 v[170:173], v239, s[56:57]
	global_load_dwordx4 v[174:177], v239, s[56:57] offset:512
	s_add_u32 s56, s56, 0x4000
	s_addc_u32 s57, s57, 0
	s_waitcnt vmcnt(8)
	s_waitcnt lgkmcnt(3)
	v_mfma_f32_32x32x16_f16 v[82:97], v[130:133], v[178:181], v[82:97]
	v_mfma_f32_32x32x16_f16 v[50:65], v[130:133], v[182:185], v[50:65]
	ds_read_b128 v[130:133], v236 offset:34944
	s_waitcnt lgkmcnt(3)
	v_mfma_f32_32x32x16_f16 v[114:129], v[134:137], v[178:181], v[114:129]
	v_mfma_f32_32x32x16_f16 v[34:49], v[134:137], v[182:185], v[34:49]
	ds_read_b128 v[134:137], v236 offset:39296
	s_waitcnt lgkmcnt(3)
	v_mfma_f32_32x32x16_f16 v[98:113], v[138:141], v[178:181], v[98:113]
	v_mfma_f32_32x32x16_f16 v[18:33], v[138:141], v[182:185], v[18:33]
	ds_read_b128 v[138:141], v236 offset:43648
	s_waitcnt lgkmcnt(3)
	v_mfma_f32_32x32x16_f16 v[66:81], v[142:145], v[178:181], v[66:81]
	v_mfma_f32_32x32x16_f16 v[2:17], v[142:145], v[182:185], v[2:17]
	ds_read_b128 v[142:145], v236 offset:48000
	s_waitcnt vmcnt(6)
	s_waitcnt lgkmcnt(3)
	v_mfma_f32_32x32x16_f16 v[82:97], v[130:133], v[146:149], v[82:97]
	v_mfma_f32_32x32x16_f16 v[50:65], v[130:133], v[150:153], v[50:65]
	ds_read_b128 v[130:133], v236 offset:34976
	s_waitcnt lgkmcnt(3)
	v_mfma_f32_32x32x16_f16 v[114:129], v[134:137], v[146:149], v[114:129]
	v_mfma_f32_32x32x16_f16 v[34:49], v[134:137], v[150:153], v[34:49]
	ds_read_b128 v[134:137], v236 offset:39328
	s_waitcnt lgkmcnt(3)
	v_mfma_f32_32x32x16_f16 v[98:113], v[138:141], v[146:149], v[98:113]
	v_mfma_f32_32x32x16_f16 v[18:33], v[138:141], v[150:153], v[18:33]
	ds_read_b128 v[138:141], v236 offset:43680
	s_waitcnt lgkmcnt(3)
	v_mfma_f32_32x32x16_f16 v[66:81], v[142:145], v[146:149], v[66:81]
	v_mfma_f32_32x32x16_f16 v[2:17], v[142:145], v[150:153], v[2:17]
	ds_read_b128 v[142:145], v236 offset:48032
	s_waitcnt vmcnt(4)
	s_waitcnt lgkmcnt(3)
	v_mfma_f32_32x32x16_f16 v[82:97], v[130:133], v[154:157], v[82:97]
	v_mfma_f32_32x32x16_f16 v[50:65], v[130:133], v[158:161], v[50:65]
	ds_read_b128 v[130:133], v236 offset:35008
	s_waitcnt lgkmcnt(3)
	v_mfma_f32_32x32x16_f16 v[114:129], v[134:137], v[154:157], v[114:129]
	v_mfma_f32_32x32x16_f16 v[34:49], v[134:137], v[158:161], v[34:49]
	ds_read_b128 v[134:137], v236 offset:39360
	s_waitcnt lgkmcnt(3)
	v_mfma_f32_32x32x16_f16 v[98:113], v[138:141], v[154:157], v[98:113]
	v_mfma_f32_32x32x16_f16 v[18:33], v[138:141], v[158:161], v[18:33]
	ds_read_b128 v[138:141], v236 offset:43712
	s_waitcnt lgkmcnt(3)
	v_mfma_f32_32x32x16_f16 v[66:81], v[142:145], v[154:157], v[66:81]
	v_mfma_f32_32x32x16_f16 v[2:17], v[142:145], v[158:161], v[2:17]
	ds_read_b128 v[142:145], v236 offset:48064
	s_waitcnt vmcnt(2)
	s_waitcnt lgkmcnt(3)
	v_mfma_f32_32x32x16_f16 v[82:97], v[130:133], v[162:165], v[82:97]
	v_mfma_f32_32x32x16_f16 v[50:65], v[130:133], v[166:169], v[50:65]
	ds_read_b128 v[130:133], v236 offset:35040
	s_waitcnt lgkmcnt(3)
	v_mfma_f32_32x32x16_f16 v[114:129], v[134:137], v[162:165], v[114:129]
	v_mfma_f32_32x32x16_f16 v[34:49], v[134:137], v[166:169], v[34:49]
	ds_read_b128 v[134:137], v236 offset:39392
	s_waitcnt lgkmcnt(3)
	v_mfma_f32_32x32x16_f16 v[98:113], v[138:141], v[162:165], v[98:113]
	v_mfma_f32_32x32x16_f16 v[18:33], v[138:141], v[166:169], v[18:33]
	ds_read_b128 v[138:141], v236 offset:43744
	s_waitcnt lgkmcnt(3)
	v_mfma_f32_32x32x16_f16 v[66:81], v[142:145], v[162:165], v[66:81]
	v_mfma_f32_32x32x16_f16 v[2:17], v[142:145], v[166:169], v[2:17]
	ds_read_b128 v[142:145], v236 offset:48096
	s_waitcnt vmcnt(0)
	s_waitcnt lgkmcnt(3)
	v_mfma_f32_32x32x16_f16 v[82:97], v[130:133], v[170:173], v[82:97]
	v_mfma_f32_32x32x16_f16 v[50:65], v[130:133], v[174:177], v[50:65]
	s_waitcnt lgkmcnt(2)
	v_mfma_f32_32x32x16_f16 v[114:129], v[134:137], v[170:173], v[114:129]
	v_mfma_f32_32x32x16_f16 v[34:49], v[134:137], v[174:177], v[34:49]
	s_waitcnt lgkmcnt(1)
	v_mfma_f32_32x32x16_f16 v[98:113], v[138:141], v[170:173], v[98:113]
	v_mfma_f32_32x32x16_f16 v[18:33], v[138:141], v[174:177], v[18:33]
	s_waitcnt lgkmcnt(0)
	v_mfma_f32_32x32x16_f16 v[66:81], v[142:145], v[170:173], v[66:81]
	v_mfma_f32_32x32x16_f16 v[2:17], v[142:145], v[174:177], v[2:17]
	s_waitcnt vmcnt(0) lgkmcnt(0)
	s_nop 15
	s_mov_b64 exec, -1
	v_bfe_u32 v202, v0, 5, 1
	s_lshl_b32 s34, s29, 9
	v_and_b32_e32 v203, 0x1c0, v0
	v_and_b32_e32 v204, 31, v0
	v_or3_b32 v0, s34, v203, v204
	v_lshlrev_b32_e32 v0, 2, v0
	s_waitcnt vmcnt(0) lgkmcnt(0)
	s_barrier
	v_mov_b32_e32 v131, v244
	v_mov_b32_e32 v1, v245
	v_fmamk_f32 v130, v131, 0x80000000, v82
	s_mov_b32 s6, 0x3dcccccd
	s_mov_b32 s7, 0xbdcccccd
	v_fma_f32 v132, v130, s6, 0
	v_fma_f32 v133, v132, s6, 0
	v_fma_f32 v130, -v133, v131, v83
	v_fmac_f32_e32 v132, 0x3dcccccd, v130
	v_fmac_f32_e32 v133, 0x3dcccccd, v132
	v_fma_f32 v130, -v133, v131, v84
	v_fmac_f32_e32 v132, 0x3dcccccd, v130
	v_fmac_f32_e32 v133, 0x3dcccccd, v132
	v_fma_f32 v130, -v133, v131, v85
	v_fmac_f32_e32 v132, 0x3dcccccd, v130
	v_fmac_f32_e32 v133, 0x3dcccccd, v132
	v_fma_f32 v130, -v133, v131, v86
	v_fmac_f32_e32 v132, 0x3dcccccd, v130
	v_fmac_f32_e32 v133, 0x3dcccccd, v132
	v_fma_f32 v130, -v133, v131, v87
	v_fmac_f32_e32 v132, 0x3dcccccd, v130
	v_fmac_f32_e32 v133, 0x3dcccccd, v132
	v_fma_f32 v130, -v133, v131, v88
	v_fmac_f32_e32 v132, 0x3dcccccd, v130
	v_fmac_f32_e32 v133, 0x3dcccccd, v132
	v_fma_f32 v130, -v133, v131, v89
	v_fmac_f32_e32 v132, 0x3dcccccd, v130
	v_fmac_f32_e32 v133, 0x3dcccccd, v132
	v_fma_f32 v130, -v133, v131, v90
	v_fmac_f32_e32 v132, 0x3dcccccd, v130
	v_fmac_f32_e32 v133, 0x3dcccccd, v132
	v_fma_f32 v130, -v133, v131, v91
	v_fmac_f32_e32 v132, 0x3dcccccd, v130
	v_fmac_f32_e32 v133, 0x3dcccccd, v132
	v_fma_f32 v130, -v133, v131, v92
	v_fmac_f32_e32 v132, 0x3dcccccd, v130
	v_fmac_f32_e32 v133, 0x3dcccccd, v132
	v_fma_f32 v130, -v133, v131, v93
	v_fmac_f32_e32 v132, 0x3dcccccd, v130
	v_fmac_f32_e32 v133, 0x3dcccccd, v132
	v_fma_f32 v130, -v133, v131, v94
	v_fmac_f32_e32 v132, 0x3dcccccd, v130
	v_fmac_f32_e32 v133, 0x3dcccccd, v132
	v_fma_f32 v130, -v133, v131, v95
	v_fmac_f32_e32 v132, 0x3dcccccd, v130
	v_fmac_f32_e32 v133, 0x3dcccccd, v132
	v_fma_f32 v130, -v133, v131, v96
	v_fmac_f32_e32 v132, 0x3dcccccd, v130
	v_fmac_f32_e32 v133, 0x3dcccccd, v132
	v_fma_f32 v130, -v133, v131, v97
	v_fmac_f32_e32 v132, 0x3dcccccd, v130
	v_fmac_f32_e32 v133, 0x3dcccccd, v132
	v_fma_f32 v130, -v133, v131, v114
	v_fmac_f32_e32 v132, 0x3dcccccd, v130
	v_fmac_f32_e32 v133, 0x3dcccccd, v132
	v_fma_f32 v130, -v133, v131, v115
	v_fmac_f32_e32 v132, 0x3dcccccd, v130
	v_fmac_f32_e32 v133, 0x3dcccccd, v132
	v_fma_f32 v130, -v133, v131, v116
	v_fmac_f32_e32 v132, 0x3dcccccd, v130
	v_fmac_f32_e32 v133, 0x3dcccccd, v132
	v_fma_f32 v130, -v133, v131, v117
	v_fmac_f32_e32 v132, 0x3dcccccd, v130
	v_fmac_f32_e32 v133, 0x3dcccccd, v132
	v_fma_f32 v130, -v133, v131, v118
	v_fmac_f32_e32 v132, 0x3dcccccd, v130
	v_fmac_f32_e32 v133, 0x3dcccccd, v132
	v_fma_f32 v130, -v133, v131, v119
	v_fmac_f32_e32 v132, 0x3dcccccd, v130
	v_fmac_f32_e32 v133, 0x3dcccccd, v132
	v_fma_f32 v130, -v133, v131, v120
	v_fmac_f32_e32 v132, 0x3dcccccd, v130
	v_fmac_f32_e32 v133, 0x3dcccccd, v132
	v_fma_f32 v130, -v133, v131, v121
	v_fmac_f32_e32 v132, 0x3dcccccd, v130
	v_fmac_f32_e32 v133, 0x3dcccccd, v132
	v_fma_f32 v130, -v133, v131, v122
	v_fmac_f32_e32 v132, 0x3dcccccd, v130
	v_fmac_f32_e32 v133, 0x3dcccccd, v132
	v_fma_f32 v130, -v133, v131, v123
	v_fmac_f32_e32 v132, 0x3dcccccd, v130
	v_fmac_f32_e32 v133, 0x3dcccccd, v132
	v_fma_f32 v130, -v133, v131, v124
	v_fmac_f32_e32 v132, 0x3dcccccd, v130
	v_fmac_f32_e32 v133, 0x3dcccccd, v132
	v_fma_f32 v130, -v133, v131, v125
	v_fmac_f32_e32 v132, 0x3dcccccd, v130
	v_fmac_f32_e32 v133, 0x3dcccccd, v132
	v_fma_f32 v130, -v133, v131, v126
	v_fmac_f32_e32 v132, 0x3dcccccd, v130
	v_fmac_f32_e32 v133, 0x3dcccccd, v132
	v_fma_f32 v130, -v133, v131, v127
	v_fmac_f32_e32 v132, 0x3dcccccd, v130
	v_fmac_f32_e32 v133, 0x3dcccccd, v132
	v_fma_f32 v130, -v133, v131, v128
	v_fmac_f32_e32 v132, 0x3dcccccd, v130
	v_fmac_f32_e32 v133, 0x3dcccccd, v132
	v_fma_f32 v130, -v133, v131, v129
	v_fmac_f32_e32 v132, 0x3dcccccd, v130
	v_fmac_f32_e32 v133, 0x3dcccccd, v132
	v_fma_f32 v130, -v133, v131, v98
	v_fmac_f32_e32 v132, 0x3dcccccd, v130
	v_fmac_f32_e32 v133, 0x3dcccccd, v132
	v_fma_f32 v130, -v133, v131, v99
	v_fmac_f32_e32 v132, 0x3dcccccd, v130
	v_fmac_f32_e32 v133, 0x3dcccccd, v132
	v_fma_f32 v130, -v133, v131, v100
	v_fmac_f32_e32 v132, 0x3dcccccd, v130
	v_fmac_f32_e32 v133, 0x3dcccccd, v132
	v_fma_f32 v130, -v133, v131, v101
	v_fmac_f32_e32 v132, 0x3dcccccd, v130
	v_fmac_f32_e32 v133, 0x3dcccccd, v132
	v_fma_f32 v130, -v133, v131, v102
	v_fmac_f32_e32 v132, 0x3dcccccd, v130
	v_fmac_f32_e32 v133, 0x3dcccccd, v132
	v_fma_f32 v130, -v133, v131, v103
	v_fmac_f32_e32 v132, 0x3dcccccd, v130
	v_fmac_f32_e32 v133, 0x3dcccccd, v132
	v_fma_f32 v130, -v133, v131, v104
	v_fmac_f32_e32 v132, 0x3dcccccd, v130
	v_fmac_f32_e32 v133, 0x3dcccccd, v132
	v_fma_f32 v130, -v133, v131, v105
	v_fmac_f32_e32 v132, 0x3dcccccd, v130
	v_fmac_f32_e32 v133, 0x3dcccccd, v132
	v_fma_f32 v130, -v133, v131, v106
	v_fmac_f32_e32 v132, 0x3dcccccd, v130
	v_fmac_f32_e32 v133, 0x3dcccccd, v132
	v_fma_f32 v130, -v133, v131, v107
	v_fmac_f32_e32 v132, 0x3dcccccd, v130
	v_fmac_f32_e32 v133, 0x3dcccccd, v132
	v_fma_f32 v130, -v133, v131, v108
	v_fmac_f32_e32 v132, 0x3dcccccd, v130
	v_fmac_f32_e32 v133, 0x3dcccccd, v132
	v_fma_f32 v130, -v133, v131, v109
	v_fmac_f32_e32 v132, 0x3dcccccd, v130
	v_fmac_f32_e32 v133, 0x3dcccccd, v132
	v_fma_f32 v130, -v133, v131, v110
	v_fmac_f32_e32 v132, 0x3dcccccd, v130
	v_fmac_f32_e32 v133, 0x3dcccccd, v132
	v_fma_f32 v130, -v133, v131, v111
	v_fmac_f32_e32 v132, 0x3dcccccd, v130
	v_fmac_f32_e32 v133, 0x3dcccccd, v132
	v_fma_f32 v130, -v133, v131, v112
	v_fmac_f32_e32 v132, 0x3dcccccd, v130
	v_fmac_f32_e32 v133, 0x3dcccccd, v132
	v_fma_f32 v130, -v133, v131, v113
	v_fmac_f32_e32 v132, 0x3dcccccd, v130
	v_fmac_f32_e32 v133, 0x3dcccccd, v132
	v_fma_f32 v130, -v133, v131, v66
	v_fmac_f32_e32 v132, 0x3dcccccd, v130
	v_fmac_f32_e32 v133, 0x3dcccccd, v132
	v_fma_f32 v130, -v133, v131, v67
	v_fmac_f32_e32 v132, 0x3dcccccd, v130
	v_fmac_f32_e32 v133, 0x3dcccccd, v132
	v_fma_f32 v130, -v133, v131, v68
	v_fmac_f32_e32 v132, 0x3dcccccd, v130
	v_fmac_f32_e32 v133, 0x3dcccccd, v132
	v_fma_f32 v130, -v133, v131, v69
	v_fmac_f32_e32 v132, 0x3dcccccd, v130
	v_fmac_f32_e32 v133, 0x3dcccccd, v132
	v_fma_f32 v130, -v133, v131, v70
	v_fmac_f32_e32 v132, 0x3dcccccd, v130
	v_fmac_f32_e32 v133, 0x3dcccccd, v132
	v_fma_f32 v130, -v133, v131, v71
	v_fmac_f32_e32 v132, 0x3dcccccd, v130
	v_fmac_f32_e32 v133, 0x3dcccccd, v132
	v_fma_f32 v130, -v133, v131, v72
	v_fmac_f32_e32 v132, 0x3dcccccd, v130
	v_fmac_f32_e32 v133, 0x3dcccccd, v132
	v_fma_f32 v130, -v133, v131, v73
	v_fmac_f32_e32 v132, 0x3dcccccd, v130
	v_fmac_f32_e32 v133, 0x3dcccccd, v132
	v_fma_f32 v130, -v133, v131, v74
	v_fmac_f32_e32 v132, 0x3dcccccd, v130
	v_fmac_f32_e32 v133, 0x3dcccccd, v132
	v_fma_f32 v130, -v133, v131, v75
	v_fmac_f32_e32 v132, 0x3dcccccd, v130
	v_fmac_f32_e32 v133, 0x3dcccccd, v132
	v_fma_f32 v130, -v133, v131, v76
	v_fmac_f32_e32 v132, 0x3dcccccd, v130
	v_fmac_f32_e32 v133, 0x3dcccccd, v132
	v_fma_f32 v130, -v133, v131, v77
	v_fmac_f32_e32 v132, 0x3dcccccd, v130
	v_fmac_f32_e32 v133, 0x3dcccccd, v132
	v_fma_f32 v130, -v133, v131, v78
	v_fmac_f32_e32 v132, 0x3dcccccd, v130
	v_fmac_f32_e32 v133, 0x3dcccccd, v132
	v_fma_f32 v130, -v133, v131, v79
	v_fmac_f32_e32 v132, 0x3dcccccd, v130
	v_fmac_f32_e32 v133, 0x3dcccccd, v132
	v_fma_f32 v130, -v133, v131, v80
	v_fmac_f32_e32 v132, 0x3dcccccd, v130
	v_fmac_f32_e32 v133, 0x3dcccccd, v132
	v_fma_f32 v130, -v133, v131, v81
	v_fmac_f32_e32 v132, 0x3dcccccd, v130
	v_fmamk_f32 v130, v1, 0x80000000, v50
	v_fma_f32 v134, v130, s6, 0
	v_fma_f32 v135, v134, s6, 0
	v_fma_f32 v130, -v135, v1, v51
	v_fmac_f32_e32 v134, 0x3dcccccd, v130
	v_fmac_f32_e32 v135, 0x3dcccccd, v134
	v_fma_f32 v130, -v135, v1, v52
	v_fmac_f32_e32 v134, 0x3dcccccd, v130
	v_fmac_f32_e32 v135, 0x3dcccccd, v134
	v_fma_f32 v130, -v135, v1, v53
	v_fmac_f32_e32 v134, 0x3dcccccd, v130
	v_fmac_f32_e32 v135, 0x3dcccccd, v134
	v_fma_f32 v130, -v135, v1, v54
	v_fmac_f32_e32 v134, 0x3dcccccd, v130
	v_fmac_f32_e32 v135, 0x3dcccccd, v134
	v_fma_f32 v130, -v135, v1, v55
	v_fmac_f32_e32 v134, 0x3dcccccd, v130
	v_fmac_f32_e32 v135, 0x3dcccccd, v134
	v_fma_f32 v130, -v135, v1, v56
	v_fmac_f32_e32 v134, 0x3dcccccd, v130
	v_fmac_f32_e32 v135, 0x3dcccccd, v134
	v_fma_f32 v130, -v135, v1, v57
	v_fmac_f32_e32 v134, 0x3dcccccd, v130
	v_fmac_f32_e32 v135, 0x3dcccccd, v134
	v_fma_f32 v130, -v135, v1, v58
	v_fmac_f32_e32 v134, 0x3dcccccd, v130
	v_fmac_f32_e32 v135, 0x3dcccccd, v134
	v_fma_f32 v130, -v135, v1, v59
	v_fmac_f32_e32 v134, 0x3dcccccd, v130
	v_fmac_f32_e32 v135, 0x3dcccccd, v134
	v_fma_f32 v130, -v135, v1, v60
	v_fmac_f32_e32 v134, 0x3dcccccd, v130
	v_fmac_f32_e32 v135, 0x3dcccccd, v134
	v_fma_f32 v130, -v135, v1, v61
	v_fmac_f32_e32 v134, 0x3dcccccd, v130
	v_fmac_f32_e32 v135, 0x3dcccccd, v134
	v_fma_f32 v130, -v135, v1, v62
	v_fmac_f32_e32 v134, 0x3dcccccd, v130
	v_fmac_f32_e32 v135, 0x3dcccccd, v134
	v_fma_f32 v130, -v135, v1, v63
	v_fmac_f32_e32 v134, 0x3dcccccd, v130
	v_fmac_f32_e32 v135, 0x3dcccccd, v134
	v_fma_f32 v130, -v135, v1, v64
	v_fmac_f32_e32 v134, 0x3dcccccd, v130
	v_fmac_f32_e32 v135, 0x3dcccccd, v134
	v_fma_f32 v130, -v135, v1, v65
	v_fmac_f32_e32 v134, 0x3dcccccd, v130
	v_fmac_f32_e32 v135, 0x3dcccccd, v134
	v_fma_f32 v130, -v135, v1, v34
	v_fmac_f32_e32 v134, 0x3dcccccd, v130
	v_fmac_f32_e32 v135, 0x3dcccccd, v134
	v_fma_f32 v130, -v135, v1, v35
	v_fmac_f32_e32 v134, 0x3dcccccd, v130
	v_fmac_f32_e32 v135, 0x3dcccccd, v134
	v_fma_f32 v130, -v135, v1, v36
	v_fmac_f32_e32 v134, 0x3dcccccd, v130
	v_fmac_f32_e32 v135, 0x3dcccccd, v134
	v_fma_f32 v130, -v135, v1, v37
	v_fmac_f32_e32 v134, 0x3dcccccd, v130
	v_fmac_f32_e32 v135, 0x3dcccccd, v134
	v_fma_f32 v130, -v135, v1, v38
	v_fmac_f32_e32 v134, 0x3dcccccd, v130
	v_fmac_f32_e32 v135, 0x3dcccccd, v134
	v_fma_f32 v130, -v135, v1, v39
	v_fmac_f32_e32 v134, 0x3dcccccd, v130
	v_fmac_f32_e32 v135, 0x3dcccccd, v134
	v_fma_f32 v130, -v135, v1, v40
	v_fmac_f32_e32 v134, 0x3dcccccd, v130
	v_fmac_f32_e32 v135, 0x3dcccccd, v134
	v_fma_f32 v130, -v135, v1, v41
	v_fmac_f32_e32 v134, 0x3dcccccd, v130
	v_fmac_f32_e32 v135, 0x3dcccccd, v134
	v_fma_f32 v130, -v135, v1, v42
	v_fmac_f32_e32 v134, 0x3dcccccd, v130
	v_fmac_f32_e32 v135, 0x3dcccccd, v134
	v_fma_f32 v130, -v135, v1, v43
	v_fmac_f32_e32 v134, 0x3dcccccd, v130
	v_fmac_f32_e32 v135, 0x3dcccccd, v134
	v_fma_f32 v130, -v135, v1, v44
	v_fmac_f32_e32 v134, 0x3dcccccd, v130
	v_fmac_f32_e32 v135, 0x3dcccccd, v134
	v_fma_f32 v130, -v135, v1, v45
	v_fmac_f32_e32 v134, 0x3dcccccd, v130
	v_fmac_f32_e32 v135, 0x3dcccccd, v134
	v_fma_f32 v130, -v135, v1, v46
	v_fmac_f32_e32 v134, 0x3dcccccd, v130
	v_fmac_f32_e32 v135, 0x3dcccccd, v134
	v_fma_f32 v130, -v135, v1, v47
	v_fmac_f32_e32 v134, 0x3dcccccd, v130
	v_fmac_f32_e32 v135, 0x3dcccccd, v134
	v_fma_f32 v130, -v135, v1, v48
	v_fmac_f32_e32 v134, 0x3dcccccd, v130
	v_fmac_f32_e32 v135, 0x3dcccccd, v134
	v_fma_f32 v130, -v135, v1, v49
	v_fmac_f32_e32 v134, 0x3dcccccd, v130
	v_fmac_f32_e32 v135, 0x3dcccccd, v134
	v_fma_f32 v130, -v135, v1, v18
	v_fmac_f32_e32 v134, 0x3dcccccd, v130
	v_fmac_f32_e32 v135, 0x3dcccccd, v134
	v_fma_f32 v130, -v135, v1, v19
	v_fmac_f32_e32 v134, 0x3dcccccd, v130
	v_fmac_f32_e32 v135, 0x3dcccccd, v134
	v_fma_f32 v130, -v135, v1, v20
	v_fmac_f32_e32 v134, 0x3dcccccd, v130
	v_fmac_f32_e32 v135, 0x3dcccccd, v134
	v_fma_f32 v130, -v135, v1, v21
	v_fmac_f32_e32 v134, 0x3dcccccd, v130
	v_fmac_f32_e32 v135, 0x3dcccccd, v134
	v_fma_f32 v130, -v135, v1, v22
	v_fmac_f32_e32 v134, 0x3dcccccd, v130
	v_fmac_f32_e32 v135, 0x3dcccccd, v134
	v_fma_f32 v130, -v135, v1, v23
	v_fmac_f32_e32 v134, 0x3dcccccd, v130
	v_fmac_f32_e32 v135, 0x3dcccccd, v134
	v_fma_f32 v130, -v135, v1, v24
	v_fmac_f32_e32 v134, 0x3dcccccd, v130
	v_fmac_f32_e32 v135, 0x3dcccccd, v134
	v_fma_f32 v130, -v135, v1, v25
	v_fmac_f32_e32 v134, 0x3dcccccd, v130
	v_fmac_f32_e32 v135, 0x3dcccccd, v134
	v_fma_f32 v130, -v135, v1, v26
	v_fmac_f32_e32 v134, 0x3dcccccd, v130
	v_fmac_f32_e32 v135, 0x3dcccccd, v134
	v_fma_f32 v130, -v135, v1, v27
	v_fmac_f32_e32 v134, 0x3dcccccd, v130
	v_fmac_f32_e32 v135, 0x3dcccccd, v134
	v_fma_f32 v130, -v135, v1, v28
	v_fmac_f32_e32 v134, 0x3dcccccd, v130
	v_fmac_f32_e32 v135, 0x3dcccccd, v134
	v_fma_f32 v130, -v135, v1, v29
	v_fmac_f32_e32 v134, 0x3dcccccd, v130
	v_fmac_f32_e32 v135, 0x3dcccccd, v134
	v_fma_f32 v130, -v135, v1, v30
	v_fmac_f32_e32 v134, 0x3dcccccd, v130
	v_fmac_f32_e32 v135, 0x3dcccccd, v134
	v_fma_f32 v130, -v135, v1, v31
	v_fmac_f32_e32 v134, 0x3dcccccd, v130
	v_fmac_f32_e32 v135, 0x3dcccccd, v134
	v_fma_f32 v130, -v135, v1, v32
	v_fmac_f32_e32 v134, 0x3dcccccd, v130
	v_fmac_f32_e32 v135, 0x3dcccccd, v134
	v_fma_f32 v130, -v135, v1, v33
	v_fmac_f32_e32 v134, 0x3dcccccd, v130
	v_fmac_f32_e32 v135, 0x3dcccccd, v134
	v_fma_f32 v130, -v135, v1, v2
	v_fmac_f32_e32 v134, 0x3dcccccd, v130
	v_fmac_f32_e32 v135, 0x3dcccccd, v134
	v_fma_f32 v130, -v135, v1, v3
	v_fmac_f32_e32 v134, 0x3dcccccd, v130
	v_fmac_f32_e32 v135, 0x3dcccccd, v134
	v_fma_f32 v130, -v135, v1, v4
	v_fmac_f32_e32 v134, 0x3dcccccd, v130
	v_fmac_f32_e32 v135, 0x3dcccccd, v134
	v_fma_f32 v130, -v135, v1, v5
	v_fmac_f32_e32 v134, 0x3dcccccd, v130
	v_fmac_f32_e32 v135, 0x3dcccccd, v134
	v_fma_f32 v130, -v135, v1, v6
	v_fmac_f32_e32 v134, 0x3dcccccd, v130
	v_fmac_f32_e32 v135, 0x3dcccccd, v134
	v_fma_f32 v130, -v135, v1, v7
	v_fmac_f32_e32 v134, 0x3dcccccd, v130
	v_fmac_f32_e32 v135, 0x3dcccccd, v134
	v_fma_f32 v130, -v135, v1, v8
	v_fmac_f32_e32 v134, 0x3dcccccd, v130
	v_fmac_f32_e32 v135, 0x3dcccccd, v134
	v_fma_f32 v130, -v135, v1, v9
	v_fmac_f32_e32 v134, 0x3dcccccd, v130
	v_fmac_f32_e32 v135, 0x3dcccccd, v134
	v_fma_f32 v130, -v135, v1, v10
	v_fmac_f32_e32 v134, 0x3dcccccd, v130
	v_fmac_f32_e32 v135, 0x3dcccccd, v134
	v_fma_f32 v130, -v135, v1, v11
	v_fmac_f32_e32 v134, 0x3dcccccd, v130
	v_fmac_f32_e32 v135, 0x3dcccccd, v134
	v_fma_f32 v130, -v135, v1, v12
	v_fmac_f32_e32 v134, 0x3dcccccd, v130
	v_fmac_f32_e32 v135, 0x3dcccccd, v134
	v_fma_f32 v130, -v135, v1, v13
	v_fmac_f32_e32 v134, 0x3dcccccd, v130
	v_fmac_f32_e32 v135, 0x3dcccccd, v134
	v_fma_f32 v130, -v135, v1, v14
	v_fmac_f32_e32 v134, 0x3dcccccd, v130
	v_fmac_f32_e32 v135, 0x3dcccccd, v134
	v_fma_f32 v130, -v135, v1, v15
	v_fmac_f32_e32 v134, 0x3dcccccd, v130
	v_fmac_f32_e32 v135, 0x3dcccccd, v134
	v_fma_f32 v130, -v135, v1, v16
	v_fmac_f32_e32 v134, 0x3dcccccd, v130
	v_fmac_f32_e32 v135, 0x3dcccccd, v134
	v_lshlrev_b32_e32 v142, 3, v203
	v_lshlrev_b32_e32 v140, 3, v204
	v_fma_f32 v130, -v135, v1, v17
	v_add3_u32 v150, 0, v142, v140
	v_fmac_f32_e32 v134, 0x3dcccccd, v130
	s_mov_b32 s10, 0xbc23d70b
	v_lshl_add_u32 v0, v202, 12, v150
	v_fmac_f32_e32 v133, 0x3dcccccd, v132
	v_fmac_f32_e32 v135, 0x3dcccccd, v134
	v_fma_f32 v130, v131, s10, 1.0
	ds_write2_b64 v0, v[132:133], v[134:135] offset1:32
	v_pk_mul_f32 v[132:133], v[130:131], s[6:7]
	s_lshl_b64 s[2:3], s[2:3], 13
	v_mov_b32_e32 v132, v130
	v_pk_mul_f32 v[136:137], v[132:133], s[6:7] op_sel_hi:[1,0]
	v_pk_mul_f32 v[138:139], v[130:131], v[132:133] op_sel_hi:[0,1]
	v_add_f32_e32 v0, 1.0, v137
	v_mov_b32_e32 v136, v137
	v_mov_b32_e32 v137, v133
	v_pk_fma_f32 v[144:145], v[130:131], v[132:133], v[136:137] op_sel_hi:[0,1,1]
	v_mov_b32_e32 v136, 0x3dcccccd
	v_mov_b32_e32 v137, v139
	v_pk_fma_f32 v[146:147], v[130:131], s[6:7], v[136:137]
	v_mov_b32_e32 v137, v138
	v_pk_fma_f32 v[132:133], v[132:133], s[6:7], v[136:137] op_sel_hi:[1,0,1]
	v_mov_b32_e32 v152, v144
	v_pk_mul_f32 v[132:133], v[144:145], v[132:133]
	v_mov_b32_e32 v145, v147
	v_mov_b32_e32 v153, v146
	v_mov_b32_e32 v138, v147
	v_mov_b32_e32 v139, v0
	v_mov_b32_e32 v148, v146
	v_mov_b32_e32 v149, v0
	v_pk_mul_f32 v[144:145], v[144:145], v[152:153]
	v_pk_fma_f32 v[132:133], v[0:1], v[146:147], v[132:133] op_sel_hi:[0,1,1]
	v_pk_fma_f32 v[138:139], v[138:139], v[148:149], v[144:145]
	s_add_u32 s8, s4, s2
	v_pk_mul_f32 v[144:145], v[132:133], v[138:139] op_sel_hi:[1,0]
	s_waitcnt lgkmcnt(0)
	v_pk_fma_f32 v[144:145], v[138:139], v[132:133], v[144:145] op_sel:[1,0,0]
	v_pk_mul_f32 v[132:133], v[132:133], v[132:133] op_sel:[1,0] op_sel_hi:[1,0]
	s_barrier
	v_pk_fma_f32 v[132:133], v[138:139], v[138:139], v[132:133]
	s_nop 0
	v_pk_mul_f32 v[138:139], v[144:145], v[132:133] op_sel_hi:[1,0]
	s_addc_u32 s3, s5, s3
	v_pk_fma_f32 v[138:139], v[132:133], v[144:145], v[138:139] op_sel:[1,0,0]
	v_pk_mul_f32 v[144:145], v[144:145], v[144:145] op_sel:[1,0] op_sel_hi:[1,0]
	s_lshl_b32 s2, s34, 3
	v_pk_fma_f32 v[132:133], v[132:133], v[132:133], v[144:145]
	ds_read_b64 v[148:149], v150
	v_pk_mul_f32 v[144:145], v[138:139], v[132:133] op_sel_hi:[1,0]
	s_add_u32 s8, s8, s2
	v_pk_fma_f32 v[144:145], v[132:133], v[138:139], v[144:145] op_sel:[1,0,0]
	v_pk_mul_f32 v[138:139], v[138:139], v[138:139] op_sel:[1,0] op_sel_hi:[1,0]
	v_mov_b32_e32 v143, 0
	v_pk_fma_f32 v[132:133], v[132:133], v[132:133], v[138:139]
	s_addc_u32 s9, s3, 0
	v_pk_mul_f32 v[138:139], v[132:133], v[132:133]
	v_pk_mul_f32 v[146:147], v[144:145], v[132:133] op_sel_hi:[1,0]
	v_mov_b32_e32 v141, v143
	v_pk_fma_f32 v[132:133], v[132:133], v[144:145], v[146:147] op_sel:[1,0,0]
	v_pk_fma_f32 v[146:147], v[144:145], v[144:145], v[138:139] op_sel:[1,0,0] op_sel_hi:[1,0,1]
	v_lshl_add_u64 v[138:139], s[8:9], 0, v[142:143]
	v_mov_b32_e32 v135, 1.0
	v_cmp_eq_u32_e64 s[0:1], 0, v202
	v_cmp_ne_u32_e32 vcc, 0, v202
	v_lshl_add_u64 v[144:145], v[138:139], 0, v[140:141]
	s_and_saveexec_b64 s[8:9], vcc
	s_cbranch_execz .LBB1_18
	ds_read_b64 v[138:139], v150 offset:4096
	v_mov_b32_e32 v152, v147
	v_mov_b32_e32 v153, v133
	s_waitcnt lgkmcnt(1)
	v_pk_mul_f32 v[152:153], v[148:149], v[152:153]
	s_nop 0
	v_add_f32_e32 v0, v152, v153
	v_mov_b32_e32 v152, v132
	v_mov_b32_e32 v153, v146
	v_pk_mul_f32 v[152:153], v[148:149], v[152:153]
	s_waitcnt lgkmcnt(0)
	v_add_f32_e32 v0, v138, v0
	v_add_f32_e32 v130, v152, v153
	v_add_f32_e32 v130, v139, v130
	v_or_b32_e32 v139, 1, v130
	v_or_b32_e32 v138, 1, v0
	global_store_dwordx2 v[144:145], v[138:139], off sc1

	.amdhsa_kernel _Z9fused_oscPKfS0_PK15HIP_vector_typeIjLj4EEPfPyPj
		.amdhsa_group_segment_fixed_size 0
		.amdhsa_private_segment_fixed_size 0
		.amdhsa_kernarg_size 48
		.amdhsa_user_sgpr_count 2
		.amdhsa_user_sgpr_dispatch_ptr 0
		.amdhsa_user_sgpr_queue_ptr 0
		.amdhsa_user_sgpr_kernarg_segment_ptr 1
		.amdhsa_user_sgpr_dispatch_id 0
		.amdhsa_user_sgpr_kernarg_preload_length 0
		.amdhsa_user_sgpr_kernarg_preload_offset 0
		.amdhsa_user_sgpr_private_segment_size 0
		.amdhsa_uses_dynamic_stack 0
		.amdhsa_enable_private_segment 0
		.amdhsa_system_sgpr_workgroup_id_x 1
		.amdhsa_system_sgpr_workgroup_id_y 0
		.amdhsa_system_sgpr_workgroup_id_z 0
		.amdhsa_system_sgpr_workgroup_info 0
		.amdhsa_system_vgpr_workitem_id 0
		.amdhsa_next_free_vgpr 256
		.amdhsa_next_free_sgpr 60
		.amdhsa_accum_offset 256
		.amdhsa_reserve_vcc 1
		.amdhsa_float_round_mode_32 0
		.amdhsa_float_round_mode_16_64 0
		.amdhsa_float_denorm_mode_32 3
		.amdhsa_float_denorm_mode_16_64 3
		.amdhsa_dx10_clamp 1
		.amdhsa_ieee_mode 1
		.amdhsa_fp16_overflow 0
		.amdhsa_tg_split 0
		.amdhsa_exception_fp_ieee_invalid_op 0
		.amdhsa_exception_fp_denorm_src 0
		.amdhsa_exception_fp_ieee_div_zero 0
		.amdhsa_exception_fp_ieee_overflow 0
		.amdhsa_exception_fp_ieee_underflow 0
		.amdhsa_exception_fp_ieee_inexact 0
		.amdhsa_exception_int_div_zero 0
	.end_amdhsa_kernel

amdhsa.kernels:
  - .agpr_count:     0
    .args:
      - .actual_access:  read_only
        .address_space:  global
        .offset:         0
        .size:           8
        .value_kind:     global_buffer
      - .actual_access:  write_only
        .address_space:  global
        .offset:         8
        .size:           8
        .value_kind:     global_buffer
      - .address_space:  global
        .offset:         16
        .size:           8
        .value_kind:     global_buffer
      - .address_space:  global
        .offset:         24
        .size:           8
        .value_kind:     global_buffer
    .group_segment_fixed_size: 0
    .kernarg_segment_align: 8
    .kernarg_segment_size: 32
    .language:       OpenCL C
    .language_version:
      - 2
      - 0
    .max_flat_workgroup_size: 256
    .name:           _Z9convert_wPKfP15HIP_vector_typeIjLj4EEPjPy
    .private_segment_fixed_size: 0
    .sgpr_count:     18
    .sgpr_spill_count: 0
    .symbol:         _Z9convert_wPKfP15HIP_vector_typeIjLj4EEPjPy.kd
    .uniform_work_group_size: 1
    .uses_dynamic_stack: false
    .vgpr_count:     20
    .vgpr_spill_count: 0
    .wavefront_size: 64
  - .agpr_count:     0
    .args:
      - .actual_access:  read_only
        .address_space:  global
        .offset:         0
        .size:           8
        .value_kind:     global_buffer
      - .actual_access:  read_only
        .address_space:  global
        .offset:         8
        .size:           8
        .value_kind:     global_buffer
      - .address_space:  global
        .offset:         16
        .size:           8
        .value_kind:     global_buffer
      - .actual_access:  write_only
        .address_space:  global
        .offset:         24
        .size:           8
        .value_kind:     global_buffer
      - .address_space:  global
        .offset:         32
        .size:           8
        .value_kind:     global_buffer
      - .address_space:  global
        .offset:         40
        .size:           8
        .value_kind:     global_buffer
    .group_segment_fixed_size: 0
    .kernarg_segment_align: 8
    .kernarg_segment_size: 48
    .language:       OpenCL C
    .language_version:
      - 2
      - 0
    .max_flat_workgroup_size: 512
    .name:           _Z9fused_oscPKfS0_PK15HIP_vector_typeIjLj4EEPfPyPj
    .private_segment_fixed_size: 0
    .sgpr_count:     66
    .sgpr_spill_count: 0
    .symbol:         _Z9fused_oscPKfS0_PK15HIP_vector_typeIjLj4EEPfPyPj.kd
    .uniform_work_group_size: 1
    .uses_dynamic_stack: false
    .vgpr_count:     256
    .vgpr_spill_count: 0
    .wavefront_size: 64
